# stack: LN1 gamma/beta preload + router LDS prefetch + RG-LRU gate epilogue loads batched up front
# baseline (speedup 1.0000x reference)
; __device__ __forceinline__ float bflo(unsigned w) { return __uint_as_float(w << 16); }
; __device__ __forceinline__ float bfhi(unsigned w) { return __uint_as_float(w & 0xffff0000u); }
; __device__ __forceinline__ float sigmoidf_(float x) { return __builtin_amdgcn_rcpf(1.f + __expf(-x)); }
;     __device__ __forceinline__ void operator()(AccRef acc, const pg8::Unit& u, int wr, int wc, int fr, int fq) const {
;         const int row0 = u.pm * 256 + wr * 64 + fr, ch0 = u.pn * 128 + wc * 32 + 4 * fq;
;         const int l15 = (fq * 16 + 15) * 4;
; #pragma unroll
;         for (int n = 0; n < 2; ++n) {
;             const int ch = ch0 + 16 * n;
;             const f32x4 vba = *(const f32x4*)(ba + ch), vbx = *(const f32x4*)(bx + ch), vsp = *(const f32x4*)(sp8 + ch);
; #pragma unroll
;             for (int ai = 0; ai < 2; ++ai)
; #pragma unroll
;                 for (int mp = 0; mp < 2; ++mp) {
;                     float A[8], B[8];
; #pragma unroll
;                     for (int sg = 0; sg < 2; ++sg) { const int m = 2 * mp + sg;
;                         const size_t ro = (size_t)(row0 + ai * 128 + m * 16) * RW + ch;
;                         const u32x2 xw = *(const u32x2*)(XC + ro);
;                         const float xc[4] = {bflo(xw.x), bfhi(xw.x), bflo(xw.y), bfhi(xw.y)};
;                         const f32x4 ar = acc[ai][0][m][n], ain = acc[ai][1][m][n];
; #pragma unroll
;                         for (int q = 0; q < 4; ++q) {
;                             const float r = sigmoidf_(ar[q] + vba[q]), ig = sigmoidf_(ain[q] + vbx[q]);
;                             const float la = -r * vsp[q];
;                             const float a = __expf(la);
;                             A[sg * 4 + q] = a; B[sg * 4 + q] = __builtin_amdgcn_sqrtf((1.f - a) * (1.f + a)) * (ig * xc[q]);
;                         }
;                     }
.LBB0_581:
	v_lshl_add_u32 v160, s46, 8, v147
	v_lshl_or_b32 v152, s28, 7, v169
	v_ashrrev_i32_e32 v153, 31, v152
	v_or_b32_e32 v164, 16, v160
	v_ashrrev_i32_e32 v161, 31, v160
	v_lshlrev_b64 v[96:97], 2, v[152:153]
	v_ashrrev_i32_e32 v165, 31, v164
	v_lshl_add_u64 v[162:163], v[152:153], 1, s[10:11]
	v_lshlrev_b64 v[150:151], 10, v[160:161]
	v_lshl_add_u64 v[154:155], s[12:13], 0, v[96:97]
	v_lshlrev_b64 v[148:149], 10, v[164:165]
	v_lshl_add_u64 v[88:89], v[162:163], 0, v[150:151]
	global_load_dwordx2 v[194:195], v[88:89], off
	global_load_dwordx2 v[220:221], v[88:89], off offset:32
	v_add_co_u32_e32 v186, vcc, 0x4000, v88
	s_nop 1
	v_addc_co_u32_e32 v187, vcc, 0, v89, vcc
	global_load_dwordx2 v[196:197], v[186:187], off
	global_load_dwordx2 v[222:223], v[186:187], off offset:32
	v_add_co_u32_e32 v186, vcc, 0x8000, v88
	s_nop 1
	v_addc_co_u32_e32 v187, vcc, 0, v89, vcc
	global_load_dwordx2 v[198:199], v[186:187], off
	global_load_dwordx2 v[224:225], v[186:187], off offset:32
	v_add_co_u32_e32 v186, vcc, 0xc000, v88
	s_nop 1
	v_addc_co_u32_e32 v187, vcc, 0, v89, vcc
	global_load_dwordx2 v[200:201], v[186:187], off
	global_load_dwordx2 v[226:227], v[186:187], off offset:32
	v_add_co_u32_e32 v186, vcc, 0x20000, v88
	s_nop 1
	v_addc_co_u32_e32 v187, vcc, 0, v89, vcc
	global_load_dwordx2 v[202:203], v[186:187], off
	global_load_dwordx2 v[228:229], v[186:187], off offset:32
	v_add_co_u32_e32 v186, vcc, 0x24000, v88
	s_nop 1
	v_addc_co_u32_e32 v187, vcc, 0, v89, vcc
	global_load_dwordx2 v[204:205], v[186:187], off
	global_load_dwordx2 v[230:231], v[186:187], off offset:32
	v_add_co_u32_e32 v186, vcc, 0x28000, v88
	s_nop 1
	v_addc_co_u32_e32 v187, vcc, 0, v89, vcc
	global_load_dwordx2 v[216:217], v[186:187], off
	global_load_dwordx2 v[232:233], v[186:187], off offset:32
	v_add_co_u32_e32 v186, vcc, 0x2c000, v88
	s_nop 1
	v_addc_co_u32_e32 v187, vcc, 0, v89, vcc
	global_load_dwordx2 v[218:219], v[186:187], off
	global_load_dwordx2 v[234:235], v[186:187], off offset:32
	global_load_dwordx4 v[92:95], v[154:155], off
	v_lshl_add_u64 v[156:157], s[14:15], 0, v[96:97]
	v_lshl_add_u64 v[98:99], v[162:163], 0, v[148:149]
	s_nop 0
	s_nop 0
	v_lshl_add_u64 v[158:159], s[16:17], 0, v[96:97]
	global_load_dwordx4 v[88:91], v[156:157], off
	flat_load_dwordx4 v[96:99], v[158:159]
	global_load_dwordx4 v[242:245], v[154:155], off offset:64
	global_load_dwordx4 v[246:249], v[156:157], off offset:64
	global_load_dwordx4 v[250:253], v[158:159], off offset:64
	s_waitcnt vmcnt(0)
	v_add_f32_e32 v132, v132, v92
	v_add_f32_e32 v133, v133, v93
	v_add_f32_e32 v134, v134, v94
	v_add_f32_e32 v135, v135, v95
	v_mul_f32_e32 v132, 0xbfb8aa3b, v132
	v_mul_f32_e32 v133, 0xbfb8aa3b, v133
	v_add_f32_e32 v136, v136, v88
	v_mul_f32_e32 v134, 0xbfb8aa3b, v134
	v_add_f32_e32 v137, v137, v89
	v_mul_f32_e32 v136, 0xbfb8aa3b, v136
	v_mul_f32_e32 v135, 0xbfb8aa3b, v135
	v_exp_f32_e32 v132, v132
	v_exp_f32_e32 v133, v133
	v_exp_f32_e32 v134, v134
	v_mul_f32_e32 v137, 0xbfb8aa3b, v137
	v_exp_f32_e32 v136, v136
	v_exp_f32_e32 v135, v135
	v_exp_f32_e32 v137, v137
	v_add_f32_e32 v138, v138, v90
	v_add_f32_e32 v139, v139, v91
	v_add_f32_e32 v128, v128, v92
	v_add_f32_e32 v132, 1.0, v132
	v_add_f32_e32 v133, 1.0, v133
	v_add_f32_e32 v134, 1.0, v134
	v_mul_f32_e32 v138, 0xbfb8aa3b, v138
	v_mul_f32_e32 v139, 0xbfb8aa3b, v139
	v_mul_f32_e32 v128, 0xbfb8aa3b, v128
	v_add_f32_e32 v136, 1.0, v136
	v_add_f32_e32 v135, 1.0, v135
	v_rcp_f32_e32 v132, v132
	v_rcp_f32_e32 v133, v133
	v_rcp_f32_e32 v134, v134
	v_exp_f32_e32 v138, v138
	v_exp_f32_e32 v139, v139
	v_exp_f32_e32 v128, v128
	v_add_f32_e32 v137, 1.0, v137
	v_rcp_f32_e32 v136, v136
	v_rcp_f32_e32 v135, v135
	v_rcp_f32_e32 v137, v137
	s_waitcnt lgkmcnt(0)
; __device__ __forceinline__ float bflo(unsigned w) { return __uint_as_float(w << 16); }
; __device__ __forceinline__ float bfhi(unsigned w) { return __uint_as_float(w & 0xffff0000u); }
; __device__ __forceinline__ float sigmoidf_(float x) { return __builtin_amdgcn_rcpf(1.f + __expf(-x)); }
;     __device__ __forceinline__ void operator()(AccRef acc, const pg8::Unit& u, int wr, int wc, int fr, int fq) const {
;     ...
;                     for (int sg = 0; sg < 2; ++sg) { const int m = 2 * mp + sg;
;                         const size_t ro = (size_t)(row0 + ai * 128 + m * 16) * RW + ch;
;                         const u32x2 xw = *(const u32x2*)(XC + ro);
;                         const float xc[4] = {bflo(xw.x), bfhi(xw.x), bflo(xw.y), bfhi(xw.y)};
;                         const f32x4 ar = acc[ai][0][m][n], ain = acc[ai][1][m][n];
; #pragma unroll
;                         for (int q = 0; q < 4; ++q) {
;                             const float r = sigmoidf_(ar[q] + vba[q]), ig = sigmoidf_(ain[q] + vbx[q]);
;                             const float la = -r * vsp[q];
;                             const float a = __expf(la);
;                             A[sg * 4 + q] = a; B[sg * 4 + q] = __builtin_amdgcn_sqrtf((1.f - a) * (1.f + a)) * (ig * xc[q]);
;                         }
;                     }
;     ...
;                     GATE_SCAN_STEP(1); GATE_SCAN_STEP(2); GATE_SCAN_STEP(4); GATE_SCAN_STEP(8);
	v_lshlrev_b32_e32 v171, 16, v194
	v_mul_f32_e32 v132, v96, v132
	v_mul_f32_e32 v133, v97, v133
	v_mul_f32_e32 v134, v98, v134
	v_and_b32_e32 v172, 0xffff0000, v194
	v_add_f32_e32 v138, 1.0, v138
	v_add_f32_e32 v139, 1.0, v139
	v_add_f32_e32 v128, 1.0, v128
	v_mul_f32_e32 v171, v136, v171
	v_mul_f32_e32 v135, v99, v135
	v_mul_f32_e32 v132, 0xbfb8aa3b, v132
	v_mul_f32_e32 v133, 0xbfb8aa3b, v133
	v_mul_f32_e32 v136, 0xbfb8aa3b, v134
	v_add_f32_e32 v129, v129, v93
	v_rcp_f32_e32 v138, v138
	v_rcp_f32_e32 v139, v139
	v_rcp_f32_e32 v128, v128
	v_mul_f32_e32 v175, v137, v172
	v_mul_f32_e32 v137, 0xbfb8aa3b, v135
	v_exp_f32_e32 v134, v132
	v_exp_f32_e32 v135, v133
	v_exp_f32_e32 v136, v136
	v_mul_f32_e32 v129, 0xbfb8aa3b, v129
	v_exp_f32_e32 v129, v129
	v_lshlrev_b32_e32 v174, 16, v195
	v_and_b32_e32 v173, 0xffff0000, v195
	v_mul_f32_e32 v138, v138, v174
	v_mul_f32_e32 v139, v139, v173
	v_exp_f32_e32 v137, v137
	v_sub_f32_e32 v132, 1.0, v134
	v_add_f32_e32 v133, 1.0, v134
	v_sub_f32_e32 v172, 1.0, v135
	v_add_f32_e32 v173, 1.0, v135
	v_sub_f32_e32 v174, 1.0, v136
	v_add_f32_e32 v180, 1.0, v136
	v_add_f32_e32 v124, v124, v88
	v_mul_f32_e32 v128, v96, v128
	v_mul_f32_e32 v132, v132, v133
	v_mul_f32_e32 v133, v172, v173
	v_mul_f32_e32 v172, v174, v180
	v_mul_f32_e32 v124, 0xbfb8aa3b, v124
	v_mul_f32_e32 v128, 0xbfb8aa3b, v128
	v_add_f32_e32 v129, 1.0, v129
	v_sqrt_f32_e32 v133, v133
	v_sqrt_f32_e32 v174, v172
	v_exp_f32_e32 v124, v124
	v_exp_f32_e32 v128, v128
	v_rcp_f32_e32 v129, v129
	v_sub_f32_e32 v181, 1.0, v137
	v_add_f32_e32 v182, 1.0, v137
	v_mul_f32_e32 v173, v181, v182
	v_sqrt_f32_e32 v180, v173
	v_mul_f32_e32 v173, v175, v133
	v_mul_f32_e32 v174, v138, v174
	v_add_f32_e32 v124, 1.0, v124
	v_sub_f32_e32 v133, 1.0, v128
	v_add_f32_e32 v138, 1.0, v128
	v_add_f32_e32 v125, v125, v89
	v_mul_f32_e32 v129, v97, v129
	v_rcp_f32_e32 v124, v124
	v_mul_f32_e32 v133, v133, v138
	v_mul_f32_e32 v125, 0xbfb8aa3b, v125
	v_mul_f32_e32 v129, 0xbfb8aa3b, v129
	v_add_f32_e32 v130, v130, v94
	v_sqrt_f32_e32 v133, v133
	v_exp_f32_e32 v125, v125
	v_exp_f32_e32 v129, v129
	v_mul_f32_e32 v130, 0xbfb8aa3b, v130
	v_exp_f32_e32 v130, v130
	v_lshlrev_b32_e32 v178, 16, v196
	v_mul_f32_e32 v124, v124, v178
	v_mul_f32_e32 v138, v124, v133
	v_add_f32_e32 v124, 1.0, v125
	v_sub_f32_e32 v125, 1.0, v129
	v_add_f32_e32 v133, 1.0, v129
	v_rcp_f32_e32 v124, v124
	v_mul_f32_e32 v125, v125, v133
	v_add_f32_e32 v130, 1.0, v130
	v_sqrt_f32_e32 v125, v125
	v_rcp_f32_e32 v130, v130
	v_and_b32_e32 v176, 0xffff0000, v196
	v_mul_f32_e32 v124, v124, v176
	v_mul_f32_e32 v175, v139, v180
	v_mul_f32_e32 v139, v124, v125
	v_mul_f32_e32 v125, v98, v130
	v_mul_f32_e32 v125, 0xbfb8aa3b, v125
	v_exp_f32_e32 v130, v125
	v_add_f32_e32 v125, v131, v95
	v_mul_f32_e32 v125, 0xbfb8aa3b, v125
	v_exp_f32_e32 v125, v125
	v_add_f32_e32 v126, v126, v90
	v_mul_f32_e32 v126, 0xbfb8aa3b, v126
	v_exp_f32_e32 v126, v126
	v_add_f32_e32 v125, 1.0, v125
	v_rcp_f32_e32 v125, v125
	v_add_f32_e32 v127, v127, v91
	v_add_f32_e32 v124, 1.0, v126
	v_sub_f32_e32 v126, 1.0, v130
	v_mul_f32_e32 v125, v99, v125
	v_add_f32_e32 v131, 1.0, v130
	v_mul_f32_e32 v127, 0xbfb8aa3b, v127
	v_mul_f32_e32 v125, 0xbfb8aa3b, v125
	v_mul_f32_e32 v126, v126, v131
	v_exp_f32_e32 v127, v127
	v_exp_f32_e32 v131, v125
	v_sqrt_f32_e32 v132, v132
	v_rcp_f32_e32 v124, v124
	v_sqrt_f32_e32 v125, v126
	v_add_f32_e32 v126, 1.0, v127
	v_sub_f32_e32 v127, 1.0, v131
	v_add_f32_e32 v133, 1.0, v131
	v_rcp_f32_e32 v126, v126
	v_mul_f32_e32 v127, v127, v133
	v_sqrt_f32_e32 v127, v127
	v_lshlrev_b32_e32 v179, 16, v197
	v_mul_f32_e32 v172, v171, v132
	v_and_b32_e32 v132, 0xffff0000, v197
	v_mul_f32_e32 v124, v124, v179
	v_mul_f32_e32 v176, v124, v125
	v_mul_f32_e32 v124, v126, v132
	v_mul_f32_e32 v177, v124, v127
	s_nop 1
	v_fmac_f32_dpp v172, v172, v134 row_shr:1 row_mask:0xf bank_mask:0xf
	v_fmac_f32_dpp v173, v173, v135 row_shr:1 row_mask:0xf bank_mask:0xf
	v_fmac_f32_dpp v174, v174, v136 row_shr:1 row_mask:0xf bank_mask:0xf
	v_fmac_f32_dpp v175, v175, v137 row_shr:1 row_mask:0xf bank_mask:0xf
	v_fmac_f32_dpp v138, v138, v128 row_shr:1 row_mask:0xf bank_mask:0xf
	v_fmac_f32_dpp v139, v139, v129 row_shr:1 row_mask:0xf bank_mask:0xf
	v_fmac_f32_dpp v176, v176, v130 row_shr:1 row_mask:0xf bank_mask:0xf
	v_fmac_f32_dpp v177, v177, v131 row_shr:1 row_mask:0xf bank_mask:0xf
	v_mul_f32_dpp v134, v134, v134 row_shr:1 row_mask:0xf bank_mask:0xf
	v_mul_f32_dpp v135, v135, v135 row_shr:1 row_mask:0xf bank_mask:0xf
	v_mul_f32_dpp v136, v136, v136 row_shr:1 row_mask:0xf bank_mask:0xf
	v_mul_f32_dpp v137, v137, v137 row_shr:1 row_mask:0xf bank_mask:0xf
	v_mul_f32_dpp v128, v128, v128 row_shr:1 row_mask:0xf bank_mask:0xf
	v_mul_f32_dpp v129, v129, v129 row_shr:1 row_mask:0xf bank_mask:0xf
	v_mul_f32_dpp v130, v130, v130 row_shr:1 row_mask:0xf bank_mask:0xf
	v_mul_f32_dpp v131, v131, v131 row_shr:1 row_mask:0xf bank_mask:0xf

;     __device__ __forceinline__ void operator()(AccRef acc, const pg8::Unit& u, int wr, int wc, int fr, int fq) const {
;     ...
;                     GATE_SCAN_STEP(1); GATE_SCAN_STEP(2); GATE_SCAN_STEP(4); GATE_SCAN_STEP(8);
	v_lshlrev_b64 v[132:133], 9, v[160:161]
	s_nop 1
	v_fmac_f32_dpp v172, v172, v134 row_shr:2 row_mask:0xf bank_mask:0xf
	v_fmac_f32_dpp v173, v173, v135 row_shr:2 row_mask:0xf bank_mask:0xf
	v_fmac_f32_dpp v174, v174, v136 row_shr:2 row_mask:0xf bank_mask:0xf
	v_fmac_f32_dpp v175, v175, v137 row_shr:2 row_mask:0xf bank_mask:0xf
	v_fmac_f32_dpp v138, v138, v128 row_shr:2 row_mask:0xf bank_mask:0xf
	v_fmac_f32_dpp v139, v139, v129 row_shr:2 row_mask:0xf bank_mask:0xf
	v_fmac_f32_dpp v176, v176, v130 row_shr:2 row_mask:0xf bank_mask:0xf
	v_fmac_f32_dpp v177, v177, v131 row_shr:2 row_mask:0xf bank_mask:0xf
	v_mul_f32_dpp v134, v134, v134 row_shr:2 row_mask:0xf bank_mask:0xf
	v_mul_f32_dpp v135, v135, v135 row_shr:2 row_mask:0xf bank_mask:0xf
	v_mul_f32_dpp v136, v136, v136 row_shr:2 row_mask:0xf bank_mask:0xf
	v_mul_f32_dpp v137, v137, v137 row_shr:2 row_mask:0xf bank_mask:0xf
	v_mul_f32_dpp v128, v128, v128 row_shr:2 row_mask:0xf bank_mask:0xf
	v_mul_f32_dpp v129, v129, v129 row_shr:2 row_mask:0xf bank_mask:0xf
	v_mul_f32_dpp v130, v130, v130 row_shr:2 row_mask:0xf bank_mask:0xf
	v_mul_f32_dpp v131, v131, v131 row_shr:2 row_mask:0xf bank_mask:0xf

;     __device__ __forceinline__ void operator()(AccRef acc, const pg8::Unit& u, int wr, int wc, int fr, int fq) const {
;     ...
;                     GATE_SCAN_STEP(1); GATE_SCAN_STEP(2); GATE_SCAN_STEP(4); GATE_SCAN_STEP(8);
	v_lshl_add_u64 v[182:183], v[132:133], 0, v[152:153]
	s_nop 1
	v_fmac_f32_dpp v172, v172, v134 row_shr:4 row_mask:0xf bank_mask:0xf
	v_fmac_f32_dpp v173, v173, v135 row_shr:4 row_mask:0xf bank_mask:0xf
	v_fmac_f32_dpp v174, v174, v136 row_shr:4 row_mask:0xf bank_mask:0xf
	v_fmac_f32_dpp v175, v175, v137 row_shr:4 row_mask:0xf bank_mask:0xf
	v_fmac_f32_dpp v138, v138, v128 row_shr:4 row_mask:0xf bank_mask:0xf
	v_fmac_f32_dpp v139, v139, v129 row_shr:4 row_mask:0xf bank_mask:0xf
	v_fmac_f32_dpp v176, v176, v130 row_shr:4 row_mask:0xf bank_mask:0xf
	v_fmac_f32_dpp v177, v177, v131 row_shr:4 row_mask:0xf bank_mask:0xf
	v_mul_f32_dpp v134, v134, v134 row_shr:4 row_mask:0xf bank_mask:0xf
	v_mul_f32_dpp v135, v135, v135 row_shr:4 row_mask:0xf bank_mask:0xf
	v_mul_f32_dpp v136, v136, v136 row_shr:4 row_mask:0xf bank_mask:0xf
	v_mul_f32_dpp v137, v137, v137 row_shr:4 row_mask:0xf bank_mask:0xf
	v_mul_f32_dpp v128, v128, v128 row_shr:4 row_mask:0xf bank_mask:0xf
	v_mul_f32_dpp v129, v129, v129 row_shr:4 row_mask:0xf bank_mask:0xf
	v_mul_f32_dpp v130, v130, v130 row_shr:4 row_mask:0xf bank_mask:0xf
	v_mul_f32_dpp v131, v131, v131 row_shr:4 row_mask:0xf bank_mask:0xf

;     __device__ __forceinline__ void operator()(AccRef acc, const pg8::Unit& u, int wr, int wc, int fr, int fq) const {
;     ...
;                     GATE_SCAN_STEP(1); GATE_SCAN_STEP(2); GATE_SCAN_STEP(4); GATE_SCAN_STEP(8);
	v_lshlrev_b64 v[182:183], 2, v[182:183]
	s_nop 1
	v_fmac_f32_dpp v172, v172, v134 row_shr:8 row_mask:0xf bank_mask:0xf
	v_fmac_f32_dpp v173, v173, v135 row_shr:8 row_mask:0xf bank_mask:0xf
	v_fmac_f32_dpp v174, v174, v136 row_shr:8 row_mask:0xf bank_mask:0xf
	v_fmac_f32_dpp v175, v175, v137 row_shr:8 row_mask:0xf bank_mask:0xf
	v_fmac_f32_dpp v138, v138, v128 row_shr:8 row_mask:0xf bank_mask:0xf
	v_fmac_f32_dpp v139, v139, v129 row_shr:8 row_mask:0xf bank_mask:0xf
	v_fmac_f32_dpp v176, v176, v130 row_shr:8 row_mask:0xf bank_mask:0xf
	v_fmac_f32_dpp v177, v177, v131 row_shr:8 row_mask:0xf bank_mask:0xf
	v_mul_f32_dpp v134, v134, v134 row_shr:8 row_mask:0xf bank_mask:0xf
	v_mul_f32_dpp v135, v135, v135 row_shr:8 row_mask:0xf bank_mask:0xf
	v_mul_f32_dpp v136, v136, v136 row_shr:8 row_mask:0xf bank_mask:0xf
	v_mul_f32_dpp v137, v137, v137 row_shr:8 row_mask:0xf bank_mask:0xf
	v_mul_f32_dpp v128, v128, v128 row_shr:8 row_mask:0xf bank_mask:0xf
	v_mul_f32_dpp v129, v129, v129 row_shr:8 row_mask:0xf bank_mask:0xf
	v_mul_f32_dpp v130, v130, v130 row_shr:8 row_mask:0xf bank_mask:0xf
	v_mul_f32_dpp v131, v131, v131 row_shr:8 row_mask:0xf bank_mask:0xf

;     __device__ __forceinline__ void operator()(AccRef acc, const pg8::Unit& u, int wr, int wc, int fr, int fq) const {
;     ...
; #pragma unroll
;                     for (int q = 0; q < 4; ++q) {
;                         const float A1 = __int_as_float(__builtin_amdgcn_ds_bpermute(l15, __float_as_int(A[q]))), H1 = __int_as_float(__builtin_amdgcn_ds_bpermute(l15, __float_as_int(B[q])));
;                         B[4 + q] = fmaf(A[4 + q], H1, B[4 + q]); A[4 + q] *= A1; }
; #pragma unroll
;                     for (int sg = 0; sg < 2; ++sg) { const size_t ro = (size_t)(row0 + ai * 128 + (2 * mp + sg) * 16) * RW + ch;
;                         *(f32x4*)(SA + ro) = (f32x4){A[sg * 4], A[sg * 4 + 1], A[sg * 4 + 2], A[sg * 4 + 3]}; *(f32x4*)(SB + ro) = (f32x4){B[sg * 4], B[sg * 4 + 1], B[sg * 4 + 2], B[sg * 4 + 3]}; }
;                     if (fr == 15) { const size_t so = (size_t)(u.pm * 8 + ai * 4 + wr * 2 + mp) * RW + ch;
;                         *(f32x4*)(sumA + so) = (f32x4){A[4], A[5], A[6], A[7]}; *(f32x4*)(sumH + so) = (f32x4){B[4], B[5], B[6], B[7]}; }
	ds_bpermute_b32 v124, v168, v134
	ds_bpermute_b32 v178, v168, v172
	ds_bpermute_b32 v125, v168, v135
	ds_bpermute_b32 v179, v168, v173
	ds_bpermute_b32 v126, v168, v136
	ds_bpermute_b32 v180, v168, v174
	ds_bpermute_b32 v127, v168, v137
	ds_bpermute_b32 v181, v168, v175
	v_lshl_add_u64 v[184:185], s[6:7], 0, v[182:183]
	global_store_dwordx4 v[184:185], v[134:137], off
	s_waitcnt lgkmcnt(0)
	v_pk_mul_f32 v[124:125], v[128:129], v[124:125]
	v_pk_mul_f32 v[126:127], v[130:131], v[126:127]
	v_lshl_add_u64 v[134:135], s[8:9], 0, v[182:183]
	global_store_dwordx4 v[134:135], v[172:175], off
	v_lshlrev_b64 v[134:135], 9, v[164:165]
	v_lshl_add_u64 v[136:137], v[134:135], 0, v[152:153]
	v_lshlrev_b64 v[136:137], 2, v[136:137]
	v_lshl_add_u64 v[164:165], s[6:7], 0, v[136:137]
	v_pk_fma_f32 v[130:131], v[130:131], v[180:181], v[176:177]
	v_pk_fma_f32 v[128:129], v[128:129], v[178:179], v[138:139]
	v_lshl_add_u64 v[136:137], s[8:9], 0, v[136:137]
	global_store_dwordx4 v[164:165], v[124:127], off
	global_store_dwordx4 v[136:137], v[128:131], off
	s_and_saveexec_b64 s[28:29], s[0:1]
	s_cbranch_execz .LBB0_583
	s_lshl_b32 s56, s46, 3
	s_add_i32 s74, s56, s94
	s_ashr_i32 s75, s74, 31
	s_lshl_b64 s[74:75], s[74:75], 9
	v_lshl_add_u64 v[136:137], s[74:75], 0, v[152:153]
	v_lshlrev_b64 v[136:137], 2, v[136:137]
	v_lshl_add_u64 v[138:139], s[18:19], 0, v[136:137]
	global_store_dwordx4 v[138:139], v[124:127], off
	s_nop 1
	v_lshl_add_u64 v[124:125], s[20:21], 0, v[136:137]
	global_store_dwordx4 v[124:125], v[128:131], off
; __device__ __forceinline__ float bflo(unsigned w) { return __uint_as_float(w << 16); }
; __device__ __forceinline__ float bfhi(unsigned w) { return __uint_as_float(w & 0xffff0000u); }
; __device__ __forceinline__ float sigmoidf_(float x) { return __builtin_amdgcn_rcpf(1.f + __expf(-x)); }
;     __device__ __forceinline__ void operator()(AccRef acc, const pg8::Unit& u, int wr, int wc, int fr, int fq) const {
;     ...
;                 for (int mp = 0; mp < 2; ++mp) {
;                     float A[8], B[8];
; #pragma unroll
;                     for (int sg = 0; sg < 2; ++sg) { const int m = 2 * mp + sg;
;                         const size_t ro = (size_t)(row0 + ai * 128 + m * 16) * RW + ch;
;                         const u32x2 xw = *(const u32x2*)(XC + ro);
;                         const float xc[4] = {bflo(xw.x), bfhi(xw.x), bflo(xw.y), bfhi(xw.y)};
;                         const f32x4 ar = acc[ai][0][m][n], ain = acc[ai][1][m][n];
; #pragma unroll
;                         for (int q = 0; q < 4; ++q) {
;                             const float r = sigmoidf_(ar[q] + vba[q]), ig = sigmoidf_(ain[q] + vbx[q]);
;                             const float la = -r * vsp[q];
;                             const float a = __expf(la);
;                             A[sg * 4 + q] = a; B[sg * 4 + q] = __builtin_amdgcn_sqrtf((1.f - a) * (1.f + a)) * (ig * xc[q]);
;                         }
;                     }
;     ...
;                     GATE_SCAN_STEP(1); GATE_SCAN_STEP(2); GATE_SCAN_STEP(4); GATE_SCAN_STEP(8);
.LBB0_583:
	s_or_b64 exec, exec, s[28:29]
	s_nop 0
	v_or_b32_e32 v128, 32, v160
	v_ashrrev_i32_e32 v129, 31, v128
	v_lshlrev_b64 v[124:125], 10, v[128:129]
	v_lshl_add_u64 v[126:127], v[162:163], 0, v[124:125]
	s_nop 0
	v_add_f32_e32 v120, v120, v92
	v_mul_f32_e32 v120, 0xbfb8aa3b, v120
	v_exp_f32_e32 v120, v120
	v_add_f32_e32 v121, v121, v93
	v_mul_f32_e32 v121, 0xbfb8aa3b, v121
	v_exp_f32_e32 v121, v121
	v_add_f32_e32 v120, 1.0, v120
	v_rcp_f32_e32 v120, v120
	v_add_f32_e32 v116, v116, v88
	v_mul_f32_e32 v116, 0xbfb8aa3b, v116
	v_add_f32_e32 v121, 1.0, v121
	v_mul_f32_e32 v120, v96, v120
	v_mul_f32_e32 v120, 0xbfb8aa3b, v120
	v_add_f32_e32 v122, v122, v94
	v_exp_f32_e32 v116, v116
	v_exp_f32_e32 v120, v120
	v_rcp_f32_e32 v121, v121
	v_mul_f32_e32 v122, 0xbfb8aa3b, v122
	v_exp_f32_e32 v122, v122
	v_add_f32_e32 v116, 1.0, v116
	v_sub_f32_e32 v136, 1.0, v120
	v_add_f32_e32 v137, 1.0, v120
	v_add_f32_e32 v117, v117, v89
	v_mul_f32_e32 v121, v97, v121
	v_rcp_f32_e32 v116, v116
	v_mul_f32_e32 v136, v136, v137
	v_mul_f32_e32 v117, 0xbfb8aa3b, v117
	v_mul_f32_e32 v121, 0xbfb8aa3b, v121
	v_add_f32_e32 v122, 1.0, v122
	v_add_f32_e32 v123, v123, v95
	v_sqrt_f32_e32 v136, v136
	v_exp_f32_e32 v117, v117
	v_exp_f32_e32 v121, v121
	v_rcp_f32_e32 v122, v122
	v_mul_f32_e32 v123, 0xbfb8aa3b, v123
	v_exp_f32_e32 v123, v123
	v_add_f32_e32 v117, 1.0, v117
	v_add_f32_e32 v118, v118, v90
	v_mul_f32_e32 v122, v98, v122
	v_rcp_f32_e32 v117, v117
	v_mul_f32_e32 v118, 0xbfb8aa3b, v118
	v_mul_f32_e32 v122, 0xbfb8aa3b, v122
	v_add_f32_e32 v123, 1.0, v123
	v_exp_f32_e32 v118, v118
	v_exp_f32_e32 v122, v122
	v_rcp_f32_e32 v123, v123
	v_add_f32_e32 v119, v119, v91
	v_add_f32_e32 v118, 1.0, v118
	v_rcp_f32_e32 v118, v118
	v_mul_f32_e32 v123, v99, v123
	v_mul_f32_e32 v119, 0xbfb8aa3b, v119
	v_mul_f32_e32 v123, 0xbfb8aa3b, v123
	v_exp_f32_e32 v119, v119
	v_exp_f32_e32 v123, v123
	v_add_f32_e32 v112, v112, v92
	v_mul_f32_e32 v112, 0xbfb8aa3b, v112
	v_add_f32_e32 v119, 1.0, v119
	v_rcp_f32_e32 v119, v119
	v_exp_f32_e32 v112, v112
	v_add_f32_e32 v108, v108, v88
	v_mul_f32_e32 v108, 0xbfb8aa3b, v108
	v_exp_f32_e32 v108, v108
	v_add_f32_e32 v112, 1.0, v112
	v_rcp_f32_e32 v112, v112
	v_add_f32_e32 v109, v109, v89
	v_add_f32_e32 v108, 1.0, v108
	v_rcp_f32_e32 v108, v108
	v_mul_f32_e32 v112, v96, v112
	v_mul_f32_e32 v112, 0xbfb8aa3b, v112
	v_exp_f32_e32 v112, v112
	v_mul_f32_e32 v109, 0xbfb8aa3b, v109
	v_exp_f32_e32 v109, v109
	v_lshlrev_b64 v[128:129], 9, v[128:129]
	v_lshl_add_u64 v[174:175], v[128:129], 0, v[152:153]
	v_lshlrev_b64 v[174:175], 2, v[174:175]
	v_add_f32_e32 v109, 1.0, v109
	v_rcp_f32_e32 v109, v109
	v_lshl_add_u64 v[176:177], s[6:7], 0, v[174:175]
	s_waitcnt lgkmcnt(0)
	v_lshlrev_b32_e32 v130, 16, v198
	v_mul_f32_e32 v116, v116, v130
	v_mul_f32_e32 v116, v136, v116
	v_sub_f32_e32 v130, 1.0, v121
	v_add_f32_e32 v136, 1.0, v121
	v_mul_f32_e32 v130, v130, v136
	v_sqrt_f32_e32 v130, v130
	v_and_b32_e32 v126, 0xffff0000, v198
	v_mul_f32_e32 v117, v117, v126
	v_sub_f32_e32 v126, 1.0, v122
	v_mul_f32_e32 v117, v130, v117
	v_add_f32_e32 v130, 1.0, v122
	v_mul_f32_e32 v126, v126, v130
	v_sqrt_f32_e32 v126, v126
	v_lshlrev_b32_e32 v131, 16, v199
	v_mul_f32_e32 v118, v118, v131
	v_add_f32_e32 v130, 1.0, v123
	v_mul_f32_e32 v118, v126, v118
	v_sub_f32_e32 v126, 1.0, v123
	v_mul_f32_e32 v126, v126, v130
	v_sqrt_f32_e32 v126, v126
	v_and_b32_e32 v127, 0xffff0000, v199
	v_or_b32_e32 v130, 48, v160
	v_mul_f32_e32 v119, v119, v127
	v_ashrrev_i32_e32 v131, 31, v130
	v_mul_f32_e32 v119, v126, v119
	v_lshlrev_b64 v[126:127], 10, v[130:131]
	v_lshl_add_u64 v[136:137], v[162:163], 0, v[126:127]
	s_nop 0
	s_waitcnt lgkmcnt(0)
	v_lshlrev_b32_e32 v139, 16, v200
	v_and_b32_e32 v161, 0xffff0000, v200
	v_lshlrev_b32_e32 v164, 16, v201
	v_and_b32_e32 v138, 0xffff0000, v201
	v_sub_f32_e32 v136, 1.0, v112
	v_add_f32_e32 v137, 1.0, v112
	v_mul_f32_e32 v136, v136, v137
	v_sqrt_f32_e32 v136, v136
	v_mul_f32_e32 v108, v108, v139
	v_mul_f32_e32 v109, v109, v161
	v_mul_f32_e32 v136, v136, v108
	v_add_f32_e32 v108, v113, v93
	v_mul_f32_e32 v108, 0xbfb8aa3b, v108
	v_exp_f32_e32 v108, v108
	s_nop 0
	v_add_f32_e32 v108, 1.0, v108
	v_rcp_f32_e32 v108, v108
	s_nop 0
	v_mul_f32_e32 v108, v97, v108
	v_mul_f32_e32 v108, 0xbfb8aa3b, v108
	v_exp_f32_e32 v113, v108
	s_nop 0
	v_sub_f32_e32 v108, 1.0, v113
	v_add_f32_e32 v137, 1.0, v113
	v_mul_f32_e32 v108, v108, v137
	v_sqrt_f32_e32 v108, v108
	s_nop 0
	v_mul_f32_e32 v137, v108, v109
	v_add_f32_e32 v108, v114, v94
	v_mul_f32_e32 v108, 0xbfb8aa3b, v108
	v_exp_f32_e32 v108, v108
	v_add_f32_e32 v109, v110, v90
	v_mul_f32_e32 v109, 0xbfb8aa3b, v109
	v_exp_f32_e32 v109, v109
	v_add_f32_e32 v108, 1.0, v108
	v_rcp_f32_e32 v108, v108
	v_add_f32_e32 v109, 1.0, v109
	v_rcp_f32_e32 v109, v109
	v_mul_f32_e32 v108, v98, v108
	v_mul_f32_e32 v108, 0xbfb8aa3b, v108
	v_exp_f32_e32 v114, v108
	v_mul_f32_e32 v109, v109, v164
	v_sub_f32_e32 v108, 1.0, v114
	v_add_f32_e32 v110, 1.0, v114
	v_mul_f32_e32 v108, v108, v110
	v_sqrt_f32_e32 v108, v108
	s_nop 0
	v_mul_f32_e32 v164, v108, v109
	v_add_f32_e32 v108, v115, v95
	v_mul_f32_e32 v108, 0xbfb8aa3b, v108
	v_exp_f32_e32 v108, v108
	v_add_f32_e32 v109, v111, v91
	v_mul_f32_e32 v109, 0xbfb8aa3b, v109
	v_exp_f32_e32 v109, v109
	v_add_f32_e32 v108, 1.0, v108
	v_rcp_f32_e32 v108, v108
	v_add_f32_e32 v109, 1.0, v109
	v_rcp_f32_e32 v109, v109
	v_mul_f32_e32 v108, v99, v108
	v_mul_f32_e32 v108, 0xbfb8aa3b, v108
	v_exp_f32_e32 v115, v108
	v_mul_f32_e32 v109, v109, v138
	v_sub_f32_e32 v108, 1.0, v115
	v_add_f32_e32 v110, 1.0, v115
	v_mul_f32_e32 v108, v108, v110
	v_sqrt_f32_e32 v108, v108
	s_nop 0
	v_mul_f32_e32 v165, v108, v109
	s_nop 1
	v_fmac_f32_dpp v116, v116, v120 row_shr:1 row_mask:0xf bank_mask:0xf
	v_fmac_f32_dpp v117, v117, v121 row_shr:1 row_mask:0xf bank_mask:0xf
	v_fmac_f32_dpp v118, v118, v122 row_shr:1 row_mask:0xf bank_mask:0xf
	v_fmac_f32_dpp v119, v119, v123 row_shr:1 row_mask:0xf bank_mask:0xf
	v_fmac_f32_dpp v136, v136, v112 row_shr:1 row_mask:0xf bank_mask:0xf
	v_fmac_f32_dpp v137, v137, v113 row_shr:1 row_mask:0xf bank_mask:0xf
	v_fmac_f32_dpp v164, v164, v114 row_shr:1 row_mask:0xf bank_mask:0xf
	v_fmac_f32_dpp v165, v165, v115 row_shr:1 row_mask:0xf bank_mask:0xf
	v_mul_f32_dpp v120, v120, v120 row_shr:1 row_mask:0xf bank_mask:0xf
	v_mul_f32_dpp v121, v121, v121 row_shr:1 row_mask:0xf bank_mask:0xf
	v_mul_f32_dpp v122, v122, v122 row_shr:1 row_mask:0xf bank_mask:0xf
	v_mul_f32_dpp v123, v123, v123 row_shr:1 row_mask:0xf bank_mask:0xf
	v_mul_f32_dpp v112, v112, v112 row_shr:1 row_mask:0xf bank_mask:0xf
	v_mul_f32_dpp v113, v113, v113 row_shr:1 row_mask:0xf bank_mask:0xf
	v_mul_f32_dpp v114, v114, v114 row_shr:1 row_mask:0xf bank_mask:0xf
	v_mul_f32_dpp v115, v115, v115 row_shr:1 row_mask:0xf bank_mask:0xf

;     __device__ __forceinline__ void operator()(AccRef acc, const pg8::Unit& u, int wr, int wc, int fr, int fq) const {
;     ...
;                     GATE_SCAN_STEP(1); GATE_SCAN_STEP(2); GATE_SCAN_STEP(4); GATE_SCAN_STEP(8);
	s_nop 0
	s_nop 1
	v_fmac_f32_dpp v116, v116, v120 row_shr:2 row_mask:0xf bank_mask:0xf
	v_fmac_f32_dpp v117, v117, v121 row_shr:2 row_mask:0xf bank_mask:0xf
	v_fmac_f32_dpp v118, v118, v122 row_shr:2 row_mask:0xf bank_mask:0xf
	v_fmac_f32_dpp v119, v119, v123 row_shr:2 row_mask:0xf bank_mask:0xf
	v_fmac_f32_dpp v136, v136, v112 row_shr:2 row_mask:0xf bank_mask:0xf
	v_fmac_f32_dpp v137, v137, v113 row_shr:2 row_mask:0xf bank_mask:0xf
	v_fmac_f32_dpp v164, v164, v114 row_shr:2 row_mask:0xf bank_mask:0xf
	v_fmac_f32_dpp v165, v165, v115 row_shr:2 row_mask:0xf bank_mask:0xf
	v_mul_f32_dpp v120, v120, v120 row_shr:2 row_mask:0xf bank_mask:0xf
	v_mul_f32_dpp v121, v121, v121 row_shr:2 row_mask:0xf bank_mask:0xf
	v_mul_f32_dpp v122, v122, v122 row_shr:2 row_mask:0xf bank_mask:0xf
	v_mul_f32_dpp v123, v123, v123 row_shr:2 row_mask:0xf bank_mask:0xf
	v_mul_f32_dpp v112, v112, v112 row_shr:2 row_mask:0xf bank_mask:0xf
	v_mul_f32_dpp v113, v113, v113 row_shr:2 row_mask:0xf bank_mask:0xf
	v_mul_f32_dpp v114, v114, v114 row_shr:2 row_mask:0xf bank_mask:0xf
	v_mul_f32_dpp v115, v115, v115 row_shr:2 row_mask:0xf bank_mask:0xf

;     __device__ __forceinline__ void operator()(AccRef acc, const pg8::Unit& u, int wr, int wc, int fr, int fq) const {
;     ...
;                     GATE_SCAN_STEP(1); GATE_SCAN_STEP(2); GATE_SCAN_STEP(4); GATE_SCAN_STEP(8);
	s_nop 0
	s_nop 1
	v_fmac_f32_dpp v116, v116, v120 row_shr:4 row_mask:0xf bank_mask:0xf
	v_fmac_f32_dpp v117, v117, v121 row_shr:4 row_mask:0xf bank_mask:0xf
	v_fmac_f32_dpp v118, v118, v122 row_shr:4 row_mask:0xf bank_mask:0xf
	v_fmac_f32_dpp v119, v119, v123 row_shr:4 row_mask:0xf bank_mask:0xf
	v_fmac_f32_dpp v136, v136, v112 row_shr:4 row_mask:0xf bank_mask:0xf
	v_fmac_f32_dpp v137, v137, v113 row_shr:4 row_mask:0xf bank_mask:0xf
	v_fmac_f32_dpp v164, v164, v114 row_shr:4 row_mask:0xf bank_mask:0xf
	v_fmac_f32_dpp v165, v165, v115 row_shr:4 row_mask:0xf bank_mask:0xf
	v_mul_f32_dpp v120, v120, v120 row_shr:4 row_mask:0xf bank_mask:0xf
	v_mul_f32_dpp v121, v121, v121 row_shr:4 row_mask:0xf bank_mask:0xf
	v_mul_f32_dpp v122, v122, v122 row_shr:4 row_mask:0xf bank_mask:0xf
	v_mul_f32_dpp v123, v123, v123 row_shr:4 row_mask:0xf bank_mask:0xf
	v_mul_f32_dpp v112, v112, v112 row_shr:4 row_mask:0xf bank_mask:0xf
	v_mul_f32_dpp v113, v113, v113 row_shr:4 row_mask:0xf bank_mask:0xf
	v_mul_f32_dpp v114, v114, v114 row_shr:4 row_mask:0xf bank_mask:0xf
	v_mul_f32_dpp v115, v115, v115 row_shr:4 row_mask:0xf bank_mask:0xf

;     __device__ __forceinline__ void operator()(AccRef acc, const pg8::Unit& u, int wr, int wc, int fr, int fq) const {
;     ...
;                     GATE_SCAN_STEP(1); GATE_SCAN_STEP(2); GATE_SCAN_STEP(4); GATE_SCAN_STEP(8);
	s_nop 0
	s_nop 1
	v_fmac_f32_dpp v116, v116, v120 row_shr:8 row_mask:0xf bank_mask:0xf
	v_fmac_f32_dpp v117, v117, v121 row_shr:8 row_mask:0xf bank_mask:0xf
	v_fmac_f32_dpp v118, v118, v122 row_shr:8 row_mask:0xf bank_mask:0xf
	v_fmac_f32_dpp v119, v119, v123 row_shr:8 row_mask:0xf bank_mask:0xf
	v_fmac_f32_dpp v136, v136, v112 row_shr:8 row_mask:0xf bank_mask:0xf
	v_fmac_f32_dpp v137, v137, v113 row_shr:8 row_mask:0xf bank_mask:0xf
	v_fmac_f32_dpp v164, v164, v114 row_shr:8 row_mask:0xf bank_mask:0xf
	v_fmac_f32_dpp v165, v165, v115 row_shr:8 row_mask:0xf bank_mask:0xf
	v_mul_f32_dpp v120, v120, v120 row_shr:8 row_mask:0xf bank_mask:0xf
	v_mul_f32_dpp v121, v121, v121 row_shr:8 row_mask:0xf bank_mask:0xf
	v_mul_f32_dpp v122, v122, v122 row_shr:8 row_mask:0xf bank_mask:0xf
	v_mul_f32_dpp v123, v123, v123 row_shr:8 row_mask:0xf bank_mask:0xf
	v_mul_f32_dpp v112, v112, v112 row_shr:8 row_mask:0xf bank_mask:0xf
	v_mul_f32_dpp v113, v113, v113 row_shr:8 row_mask:0xf bank_mask:0xf
	v_mul_f32_dpp v114, v114, v114 row_shr:8 row_mask:0xf bank_mask:0xf
	v_mul_f32_dpp v115, v115, v115 row_shr:8 row_mask:0xf bank_mask:0xf

;     __device__ __forceinline__ void operator()(AccRef acc, const pg8::Unit& u, int wr, int wc, int fr, int fq) const {
;     ...
; #pragma unroll
;                     for (int q = 0; q < 4; ++q) {
;                         const float A1 = __int_as_float(__builtin_amdgcn_ds_bpermute(l15, __float_as_int(A[q]))), H1 = __int_as_float(__builtin_amdgcn_ds_bpermute(l15, __float_as_int(B[q])));
;                         B[4 + q] = fmaf(A[4 + q], H1, B[4 + q]); A[4 + q] *= A1; }
; #pragma unroll
;                     for (int sg = 0; sg < 2; ++sg) { const size_t ro = (size_t)(row0 + ai * 128 + (2 * mp + sg) * 16) * RW + ch;
;                         *(f32x4*)(SA + ro) = (f32x4){A[sg * 4], A[sg * 4 + 1], A[sg * 4 + 2], A[sg * 4 + 3]}; *(f32x4*)(SB + ro) = (f32x4){B[sg * 4], B[sg * 4 + 1], B[sg * 4 + 2], B[sg * 4 + 3]}; }
;                     if (fr == 15) { const size_t so = (size_t)(u.pm * 8 + ai * 4 + wr * 2 + mp) * RW + ch;
;                         *(f32x4*)(sumA + so) = (f32x4){A[4], A[5], A[6], A[7]}; *(f32x4*)(sumH + so) = (f32x4){B[4], B[5], B[6], B[7]}; }
	ds_bpermute_b32 v108, v168, v120
	ds_bpermute_b32 v138, v168, v116
	ds_bpermute_b32 v109, v168, v121
	ds_bpermute_b32 v139, v168, v117
	ds_bpermute_b32 v110, v168, v122
	ds_bpermute_b32 v172, v168, v118
	ds_bpermute_b32 v111, v168, v123
	ds_bpermute_b32 v173, v168, v119
	global_store_dwordx4 v[176:177], v[120:123], off
	s_waitcnt lgkmcnt(0)
	v_pk_mul_f32 v[108:109], v[112:113], v[108:109]
	v_pk_fma_f32 v[112:113], v[112:113], v[138:139], v[136:137]
	v_lshl_add_u64 v[120:121], s[8:9], 0, v[174:175]
	global_store_dwordx4 v[120:121], v[116:119], off
	v_pk_mul_f32 v[110:111], v[114:115], v[110:111]
	v_pk_fma_f32 v[114:115], v[114:115], v[172:173], v[164:165]
	v_lshlrev_b64 v[116:117], 9, v[130:131]
	v_lshl_add_u64 v[118:119], v[116:117], 0, v[152:153]
	v_lshlrev_b64 v[118:119], 2, v[118:119]
	v_lshl_add_u64 v[120:121], s[6:7], 0, v[118:119]
	v_lshl_add_u64 v[118:119], s[8:9], 0, v[118:119]
	global_store_dwordx4 v[120:121], v[108:111], off
	global_store_dwordx4 v[118:119], v[112:115], off
	s_and_saveexec_b64 s[28:29], s[0:1]
	s_cbranch_execz .LBB0_585
	s_lshl_b32 s56, s46, 3
	s_add_i32 s74, s56, s95
	s_ashr_i32 s75, s74, 31
	s_lshl_b64 s[74:75], s[74:75], 9
	v_lshl_add_u64 v[118:119], s[74:75], 0, v[152:153]
	v_lshlrev_b64 v[118:119], 2, v[118:119]
	v_lshl_add_u64 v[120:121], s[18:19], 0, v[118:119]
	global_store_dwordx4 v[120:121], v[108:111], off
	s_nop 1
	v_lshl_add_u64 v[108:109], s[20:21], 0, v[118:119]
	global_store_dwordx4 v[108:109], v[112:115], off
; __device__ __forceinline__ float bflo(unsigned w) { return __uint_as_float(w << 16); }
; __device__ __forceinline__ float bfhi(unsigned w) { return __uint_as_float(w & 0xffff0000u); }
; __device__ __forceinline__ float sigmoidf_(float x) { return __builtin_amdgcn_rcpf(1.f + __expf(-x)); }
;     __device__ __forceinline__ void operator()(AccRef acc, const pg8::Unit& u, int wr, int wc, int fr, int fq) const {
;     ...
;                 for (int mp = 0; mp < 2; ++mp) {
;                     float A[8], B[8];
; #pragma unroll
;                     for (int sg = 0; sg < 2; ++sg) { const int m = 2 * mp + sg;
;                         const size_t ro = (size_t)(row0 + ai * 128 + m * 16) * RW + ch;
;                         const u32x2 xw = *(const u32x2*)(XC + ro);
;                         const float xc[4] = {bflo(xw.x), bfhi(xw.x), bflo(xw.y), bfhi(xw.y)};
;                         const f32x4 ar = acc[ai][0][m][n], ain = acc[ai][1][m][n];
; #pragma unroll
;                         for (int q = 0; q < 4; ++q) {
;                             const float r = sigmoidf_(ar[q] + vba[q]), ig = sigmoidf_(ain[q] + vbx[q]);
;                             const float la = -r * vsp[q];
;                             const float a = __expf(la);
;                             A[sg * 4 + q] = a; B[sg * 4 + q] = __builtin_amdgcn_sqrtf((1.f - a) * (1.f + a)) * (ig * xc[q]);
;                         }
;                     }
;     ...
;                     GATE_SCAN_STEP(1); GATE_SCAN_STEP(2); GATE_SCAN_STEP(4); GATE_SCAN_STEP(8);
.LBB0_585:
	s_or_b64 exec, exec, s[28:29]
	s_nop 0
	v_add_u32_e32 v112, 0x80, v160
	v_ashrrev_i32_e32 v113, 31, v112
	v_lshlrev_b64 v[108:109], 10, v[112:113]
	v_lshl_add_u64 v[110:111], v[162:163], 0, v[108:109]
	s_nop 0
	v_add_f32_e32 v104, v104, v92
	v_mul_f32_e32 v104, 0xbfb8aa3b, v104
	v_exp_f32_e32 v104, v104
	v_add_f32_e32 v105, v105, v93
	v_mul_f32_e32 v105, 0xbfb8aa3b, v105
	v_exp_f32_e32 v105, v105
	v_add_f32_e32 v104, 1.0, v104
	v_rcp_f32_e32 v104, v104
	v_add_f32_e32 v100, v100, v88
	v_mul_f32_e32 v100, 0xbfb8aa3b, v100
	v_add_f32_e32 v105, 1.0, v105
	v_mul_f32_e32 v104, v96, v104
	v_mul_f32_e32 v104, 0xbfb8aa3b, v104
	v_add_f32_e32 v106, v106, v94
	v_exp_f32_e32 v100, v100
	v_exp_f32_e32 v104, v104
	v_rcp_f32_e32 v105, v105
	v_mul_f32_e32 v106, 0xbfb8aa3b, v106
	v_exp_f32_e32 v106, v106
	v_add_f32_e32 v100, 1.0, v100
	v_sub_f32_e32 v118, 1.0, v104
	v_add_f32_e32 v119, 1.0, v104
	v_add_f32_e32 v101, v101, v89
	v_mul_f32_e32 v105, v97, v105
	v_rcp_f32_e32 v100, v100
	v_mul_f32_e32 v118, v118, v119
	v_mul_f32_e32 v101, 0xbfb8aa3b, v101
	v_mul_f32_e32 v105, 0xbfb8aa3b, v105
	v_add_f32_e32 v106, 1.0, v106
	v_add_f32_e32 v107, v107, v95
	v_sqrt_f32_e32 v118, v118
	v_exp_f32_e32 v101, v101
	v_exp_f32_e32 v105, v105
	v_rcp_f32_e32 v106, v106
	v_mul_f32_e32 v107, 0xbfb8aa3b, v107
	v_exp_f32_e32 v107, v107
	v_add_f32_e32 v101, 1.0, v101
	v_add_f32_e32 v102, v102, v90
	v_mul_f32_e32 v106, v98, v106
	v_rcp_f32_e32 v101, v101
	v_mul_f32_e32 v102, 0xbfb8aa3b, v102
	v_mul_f32_e32 v106, 0xbfb8aa3b, v106
	v_add_f32_e32 v107, 1.0, v107
	v_exp_f32_e32 v102, v102
	v_exp_f32_e32 v106, v106
	v_rcp_f32_e32 v107, v107
	v_add_f32_e32 v103, v103, v91
	v_add_f32_e32 v102, 1.0, v102
	v_rcp_f32_e32 v102, v102
	v_mul_f32_e32 v107, v99, v107
	v_mul_f32_e32 v103, 0xbfb8aa3b, v103
	v_mul_f32_e32 v107, 0xbfb8aa3b, v107
	v_exp_f32_e32 v103, v103
	v_exp_f32_e32 v107, v107
	v_add_f32_e32 v84, v84, v92
	v_mul_f32_e32 v84, 0xbfb8aa3b, v84
	v_add_f32_e32 v103, 1.0, v103
	v_rcp_f32_e32 v103, v103
	v_exp_f32_e32 v84, v84
	v_add_f32_e32 v80, v80, v88
	v_mul_f32_e32 v80, 0xbfb8aa3b, v80
	v_exp_f32_e32 v80, v80
	v_add_f32_e32 v84, 1.0, v84
	v_rcp_f32_e32 v84, v84
	v_add_f32_e32 v81, v81, v89
	v_add_f32_e32 v80, 1.0, v80
	v_rcp_f32_e32 v80, v80
	v_mul_f32_e32 v84, v96, v84
	v_mul_f32_e32 v84, 0xbfb8aa3b, v84
	v_exp_f32_e32 v84, v84
	v_mul_f32_e32 v81, 0xbfb8aa3b, v81
	v_exp_f32_e32 v81, v81
	v_lshlrev_b64 v[112:113], 9, v[112:113]
	v_lshl_add_u64 v[136:137], v[112:113], 0, v[152:153]
	v_lshlrev_b64 v[136:137], 2, v[136:137]
	v_add_f32_e32 v81, 1.0, v81
	v_rcp_f32_e32 v81, v81
	v_lshl_add_u64 v[138:139], s[6:7], 0, v[136:137]
	s_waitcnt lgkmcnt(0)
	v_lshlrev_b32_e32 v114, 16, v202
	v_mul_f32_e32 v100, v100, v114
	v_mul_f32_e32 v100, v118, v100
	v_sub_f32_e32 v114, 1.0, v105
	v_add_f32_e32 v118, 1.0, v105
	v_mul_f32_e32 v114, v114, v118
	v_sqrt_f32_e32 v114, v114
	v_and_b32_e32 v110, 0xffff0000, v202
	v_mul_f32_e32 v101, v101, v110
	v_sub_f32_e32 v110, 1.0, v106
	v_mul_f32_e32 v101, v114, v101
	v_add_f32_e32 v114, 1.0, v106
	v_mul_f32_e32 v110, v110, v114
	v_sqrt_f32_e32 v110, v110
	v_lshlrev_b32_e32 v115, 16, v203
	v_mul_f32_e32 v102, v102, v115
	v_add_f32_e32 v114, 1.0, v107
	v_mul_f32_e32 v102, v110, v102
	v_sub_f32_e32 v110, 1.0, v107
	v_mul_f32_e32 v110, v110, v114
	v_sqrt_f32_e32 v110, v110
	v_and_b32_e32 v111, 0xffff0000, v203
	v_add_u32_e32 v114, 0x90, v160
	v_mul_f32_e32 v103, v103, v111
	v_ashrrev_i32_e32 v115, 31, v114
	v_mul_f32_e32 v103, v110, v103
	v_lshlrev_b64 v[110:111], 10, v[114:115]
	v_lshl_add_u64 v[118:119], v[162:163], 0, v[110:111]
	s_nop 0
	s_waitcnt lgkmcnt(0)
	v_lshlrev_b32_e32 v121, 16, v204
	v_and_b32_e32 v122, 0xffff0000, v204
	v_lshlrev_b32_e32 v123, 16, v205
	v_and_b32_e32 v120, 0xffff0000, v205
	v_sub_f32_e32 v118, 1.0, v84
	v_add_f32_e32 v119, 1.0, v84
	v_mul_f32_e32 v118, v118, v119
	v_sqrt_f32_e32 v118, v118
	v_mul_f32_e32 v80, v80, v121
	v_mul_f32_e32 v81, v81, v122
	v_mul_f32_e32 v118, v118, v80
	v_add_f32_e32 v80, v85, v93
	v_mul_f32_e32 v80, 0xbfb8aa3b, v80
	v_exp_f32_e32 v80, v80
	s_nop 0
	v_add_f32_e32 v80, 1.0, v80
	v_rcp_f32_e32 v80, v80
	s_nop 0
	v_mul_f32_e32 v80, v97, v80
	v_mul_f32_e32 v80, 0xbfb8aa3b, v80
	v_exp_f32_e32 v85, v80
	s_nop 0
	v_sub_f32_e32 v80, 1.0, v85
	v_add_f32_e32 v119, 1.0, v85
	v_mul_f32_e32 v80, v80, v119
	v_sqrt_f32_e32 v80, v80
	s_nop 0
	v_mul_f32_e32 v119, v80, v81
	v_add_f32_e32 v80, v86, v94
	v_mul_f32_e32 v80, 0xbfb8aa3b, v80
	v_exp_f32_e32 v80, v80
	v_add_f32_e32 v81, v82, v90
	v_mul_f32_e32 v81, 0xbfb8aa3b, v81
	v_exp_f32_e32 v81, v81
	v_add_f32_e32 v80, 1.0, v80
	v_rcp_f32_e32 v80, v80
	v_add_f32_e32 v81, 1.0, v81
	v_rcp_f32_e32 v81, v81
	v_mul_f32_e32 v80, v98, v80
	v_mul_f32_e32 v80, 0xbfb8aa3b, v80
	v_exp_f32_e32 v86, v80
	v_mul_f32_e32 v81, v81, v123
	v_sub_f32_e32 v80, 1.0, v86
	v_add_f32_e32 v82, 1.0, v86
	v_mul_f32_e32 v80, v80, v82
	v_sqrt_f32_e32 v80, v80
	s_nop 0
	v_mul_f32_e32 v122, v80, v81
	v_add_f32_e32 v80, v87, v95
	v_mul_f32_e32 v80, 0xbfb8aa3b, v80
	v_exp_f32_e32 v80, v80
	v_add_f32_e32 v81, v83, v91
	v_mul_f32_e32 v81, 0xbfb8aa3b, v81
	v_exp_f32_e32 v81, v81
	v_add_f32_e32 v80, 1.0, v80
	v_rcp_f32_e32 v80, v80
	v_add_f32_e32 v81, 1.0, v81
	v_rcp_f32_e32 v81, v81
	v_mul_f32_e32 v80, v99, v80
	v_mul_f32_e32 v80, 0xbfb8aa3b, v80
	v_exp_f32_e32 v87, v80
	v_mul_f32_e32 v81, v81, v120
	v_sub_f32_e32 v80, 1.0, v87
	v_add_f32_e32 v82, 1.0, v87
	v_mul_f32_e32 v80, v80, v82
	v_sqrt_f32_e32 v80, v80
	s_nop 0
	v_mul_f32_e32 v123, v80, v81
	s_nop 1
	v_fmac_f32_dpp v100, v100, v104 row_shr:1 row_mask:0xf bank_mask:0xf
	v_fmac_f32_dpp v101, v101, v105 row_shr:1 row_mask:0xf bank_mask:0xf
	v_fmac_f32_dpp v102, v102, v106 row_shr:1 row_mask:0xf bank_mask:0xf
	v_fmac_f32_dpp v103, v103, v107 row_shr:1 row_mask:0xf bank_mask:0xf
	v_fmac_f32_dpp v118, v118, v84 row_shr:1 row_mask:0xf bank_mask:0xf
	v_fmac_f32_dpp v119, v119, v85 row_shr:1 row_mask:0xf bank_mask:0xf
	v_fmac_f32_dpp v122, v122, v86 row_shr:1 row_mask:0xf bank_mask:0xf
	v_fmac_f32_dpp v123, v123, v87 row_shr:1 row_mask:0xf bank_mask:0xf
	v_mul_f32_dpp v104, v104, v104 row_shr:1 row_mask:0xf bank_mask:0xf
	v_mul_f32_dpp v105, v105, v105 row_shr:1 row_mask:0xf bank_mask:0xf
	v_mul_f32_dpp v106, v106, v106 row_shr:1 row_mask:0xf bank_mask:0xf
	v_mul_f32_dpp v107, v107, v107 row_shr:1 row_mask:0xf bank_mask:0xf
	v_mul_f32_dpp v84, v84, v84 row_shr:1 row_mask:0xf bank_mask:0xf
	v_mul_f32_dpp v85, v85, v85 row_shr:1 row_mask:0xf bank_mask:0xf
	v_mul_f32_dpp v86, v86, v86 row_shr:1 row_mask:0xf bank_mask:0xf
	v_mul_f32_dpp v87, v87, v87 row_shr:1 row_mask:0xf bank_mask:0xf

;     __device__ __forceinline__ void operator()(AccRef acc, const pg8::Unit& u, int wr, int wc, int fr, int fq) const {
;     ...
;                     GATE_SCAN_STEP(1); GATE_SCAN_STEP(2); GATE_SCAN_STEP(4); GATE_SCAN_STEP(8);
	s_nop 0
	s_nop 1
	v_fmac_f32_dpp v100, v100, v104 row_shr:2 row_mask:0xf bank_mask:0xf
	v_fmac_f32_dpp v101, v101, v105 row_shr:2 row_mask:0xf bank_mask:0xf
	v_fmac_f32_dpp v102, v102, v106 row_shr:2 row_mask:0xf bank_mask:0xf
	v_fmac_f32_dpp v103, v103, v107 row_shr:2 row_mask:0xf bank_mask:0xf
	v_fmac_f32_dpp v118, v118, v84 row_shr:2 row_mask:0xf bank_mask:0xf
	v_fmac_f32_dpp v119, v119, v85 row_shr:2 row_mask:0xf bank_mask:0xf
	v_fmac_f32_dpp v122, v122, v86 row_shr:2 row_mask:0xf bank_mask:0xf
	v_fmac_f32_dpp v123, v123, v87 row_shr:2 row_mask:0xf bank_mask:0xf
	v_mul_f32_dpp v104, v104, v104 row_shr:2 row_mask:0xf bank_mask:0xf
	v_mul_f32_dpp v105, v105, v105 row_shr:2 row_mask:0xf bank_mask:0xf
	v_mul_f32_dpp v106, v106, v106 row_shr:2 row_mask:0xf bank_mask:0xf
	v_mul_f32_dpp v107, v107, v107 row_shr:2 row_mask:0xf bank_mask:0xf
	v_mul_f32_dpp v84, v84, v84 row_shr:2 row_mask:0xf bank_mask:0xf
	v_mul_f32_dpp v85, v85, v85 row_shr:2 row_mask:0xf bank_mask:0xf
	v_mul_f32_dpp v86, v86, v86 row_shr:2 row_mask:0xf bank_mask:0xf
	v_mul_f32_dpp v87, v87, v87 row_shr:2 row_mask:0xf bank_mask:0xf

;     __device__ __forceinline__ void operator()(AccRef acc, const pg8::Unit& u, int wr, int wc, int fr, int fq) const {
;     ...
;                     GATE_SCAN_STEP(1); GATE_SCAN_STEP(2); GATE_SCAN_STEP(4); GATE_SCAN_STEP(8);
	s_nop 0
	s_nop 1
	v_fmac_f32_dpp v100, v100, v104 row_shr:4 row_mask:0xf bank_mask:0xf
	v_fmac_f32_dpp v101, v101, v105 row_shr:4 row_mask:0xf bank_mask:0xf
	v_fmac_f32_dpp v102, v102, v106 row_shr:4 row_mask:0xf bank_mask:0xf
	v_fmac_f32_dpp v103, v103, v107 row_shr:4 row_mask:0xf bank_mask:0xf
	v_fmac_f32_dpp v118, v118, v84 row_shr:4 row_mask:0xf bank_mask:0xf
	v_fmac_f32_dpp v119, v119, v85 row_shr:4 row_mask:0xf bank_mask:0xf
	v_fmac_f32_dpp v122, v122, v86 row_shr:4 row_mask:0xf bank_mask:0xf
	v_fmac_f32_dpp v123, v123, v87 row_shr:4 row_mask:0xf bank_mask:0xf
	v_mul_f32_dpp v104, v104, v104 row_shr:4 row_mask:0xf bank_mask:0xf
	v_mul_f32_dpp v105, v105, v105 row_shr:4 row_mask:0xf bank_mask:0xf
	v_mul_f32_dpp v106, v106, v106 row_shr:4 row_mask:0xf bank_mask:0xf
	v_mul_f32_dpp v107, v107, v107 row_shr:4 row_mask:0xf bank_mask:0xf
	v_mul_f32_dpp v84, v84, v84 row_shr:4 row_mask:0xf bank_mask:0xf
	v_mul_f32_dpp v85, v85, v85 row_shr:4 row_mask:0xf bank_mask:0xf
	v_mul_f32_dpp v86, v86, v86 row_shr:4 row_mask:0xf bank_mask:0xf
	v_mul_f32_dpp v87, v87, v87 row_shr:4 row_mask:0xf bank_mask:0xf

;     __device__ __forceinline__ void operator()(AccRef acc, const pg8::Unit& u, int wr, int wc, int fr, int fq) const {
;     ...
;                     GATE_SCAN_STEP(1); GATE_SCAN_STEP(2); GATE_SCAN_STEP(4); GATE_SCAN_STEP(8);
	s_nop 0
	s_nop 1
	v_fmac_f32_dpp v100, v100, v104 row_shr:8 row_mask:0xf bank_mask:0xf
	v_fmac_f32_dpp v101, v101, v105 row_shr:8 row_mask:0xf bank_mask:0xf
	v_fmac_f32_dpp v102, v102, v106 row_shr:8 row_mask:0xf bank_mask:0xf
	v_fmac_f32_dpp v103, v103, v107 row_shr:8 row_mask:0xf bank_mask:0xf
	v_fmac_f32_dpp v118, v118, v84 row_shr:8 row_mask:0xf bank_mask:0xf
	v_fmac_f32_dpp v119, v119, v85 row_shr:8 row_mask:0xf bank_mask:0xf
	v_fmac_f32_dpp v122, v122, v86 row_shr:8 row_mask:0xf bank_mask:0xf
	v_fmac_f32_dpp v123, v123, v87 row_shr:8 row_mask:0xf bank_mask:0xf
	v_mul_f32_dpp v104, v104, v104 row_shr:8 row_mask:0xf bank_mask:0xf
	v_mul_f32_dpp v105, v105, v105 row_shr:8 row_mask:0xf bank_mask:0xf
	v_mul_f32_dpp v106, v106, v106 row_shr:8 row_mask:0xf bank_mask:0xf
	v_mul_f32_dpp v107, v107, v107 row_shr:8 row_mask:0xf bank_mask:0xf
	v_mul_f32_dpp v84, v84, v84 row_shr:8 row_mask:0xf bank_mask:0xf
	v_mul_f32_dpp v85, v85, v85 row_shr:8 row_mask:0xf bank_mask:0xf
	v_mul_f32_dpp v86, v86, v86 row_shr:8 row_mask:0xf bank_mask:0xf
	v_mul_f32_dpp v87, v87, v87 row_shr:8 row_mask:0xf bank_mask:0xf

;     __device__ __forceinline__ void operator()(AccRef acc, const pg8::Unit& u, int wr, int wc, int fr, int fq) const {
;     ...
; #pragma unroll
;                     for (int q = 0; q < 4; ++q) {
;                         const float A1 = __int_as_float(__builtin_amdgcn_ds_bpermute(l15, __float_as_int(A[q]))), H1 = __int_as_float(__builtin_amdgcn_ds_bpermute(l15, __float_as_int(B[q])));
;                         B[4 + q] = fmaf(A[4 + q], H1, B[4 + q]); A[4 + q] *= A1; }
; #pragma unroll
;                     for (int sg = 0; sg < 2; ++sg) { const size_t ro = (size_t)(row0 + ai * 128 + (2 * mp + sg) * 16) * RW + ch;
;                         *(f32x4*)(SA + ro) = (f32x4){A[sg * 4], A[sg * 4 + 1], A[sg * 4 + 2], A[sg * 4 + 3]}; *(f32x4*)(SB + ro) = (f32x4){B[sg * 4], B[sg * 4 + 1], B[sg * 4 + 2], B[sg * 4 + 3]}; }
;                     if (fr == 15) { const size_t so = (size_t)(u.pm * 8 + ai * 4 + wr * 2 + mp) * RW + ch;
;                         *(f32x4*)(sumA + so) = (f32x4){A[4], A[5], A[6], A[7]}; *(f32x4*)(sumH + so) = (f32x4){B[4], B[5], B[6], B[7]}; }
	ds_bpermute_b32 v80, v168, v104
	ds_bpermute_b32 v120, v168, v100
	ds_bpermute_b32 v81, v168, v105
	ds_bpermute_b32 v121, v168, v101
	ds_bpermute_b32 v82, v168, v106
	ds_bpermute_b32 v130, v168, v102
	ds_bpermute_b32 v83, v168, v107
	ds_bpermute_b32 v131, v168, v103
	global_store_dwordx4 v[138:139], v[104:107], off
	s_waitcnt lgkmcnt(0)
	v_pk_mul_f32 v[80:81], v[84:85], v[80:81]
	v_pk_fma_f32 v[84:85], v[84:85], v[120:121], v[118:119]
	v_lshl_add_u64 v[104:105], s[8:9], 0, v[136:137]
	global_store_dwordx4 v[104:105], v[100:103], off
	v_pk_mul_f32 v[82:83], v[86:87], v[82:83]
	v_pk_fma_f32 v[86:87], v[86:87], v[130:131], v[122:123]
	v_lshlrev_b64 v[100:101], 9, v[114:115]
	v_lshl_add_u64 v[102:103], v[100:101], 0, v[152:153]
	v_lshlrev_b64 v[102:103], 2, v[102:103]
	v_lshl_add_u64 v[104:105], s[6:7], 0, v[102:103]
	v_lshl_add_u64 v[102:103], s[8:9], 0, v[102:103]
	global_store_dwordx4 v[104:105], v[80:83], off
	global_store_dwordx4 v[102:103], v[84:87], off
	s_and_saveexec_b64 s[28:29], s[0:1]
	s_cbranch_execz .LBB0_587
	s_lshl_b32 s56, s46, 3
	s_add_i32 s74, s56, s96
	s_ashr_i32 s75, s74, 31
	s_lshl_b64 s[74:75], s[74:75], 9
	v_lshl_add_u64 v[102:103], s[74:75], 0, v[152:153]
	v_lshlrev_b64 v[102:103], 2, v[102:103]
	v_lshl_add_u64 v[104:105], s[18:19], 0, v[102:103]
	global_store_dwordx4 v[104:105], v[80:83], off
	s_nop 1
	v_lshl_add_u64 v[80:81], s[20:21], 0, v[102:103]
	global_store_dwordx4 v[80:81], v[84:87], off
; __device__ __forceinline__ float bflo(unsigned w) { return __uint_as_float(w << 16); }
; __device__ __forceinline__ float bfhi(unsigned w) { return __uint_as_float(w & 0xffff0000u); }
; __device__ __forceinline__ float sigmoidf_(float x) { return __builtin_amdgcn_rcpf(1.f + __expf(-x)); }
;     __device__ __forceinline__ void operator()(AccRef acc, const pg8::Unit& u, int wr, int wc, int fr, int fq) const {
;     ...
;                 for (int mp = 0; mp < 2; ++mp) {
;                     float A[8], B[8];
; #pragma unroll
;                     for (int sg = 0; sg < 2; ++sg) { const int m = 2 * mp + sg;
;                         const size_t ro = (size_t)(row0 + ai * 128 + m * 16) * RW + ch;
;                         const u32x2 xw = *(const u32x2*)(XC + ro);
;                         const float xc[4] = {bflo(xw.x), bfhi(xw.x), bflo(xw.y), bfhi(xw.y)};
;                         const f32x4 ar = acc[ai][0][m][n], ain = acc[ai][1][m][n];
; #pragma unroll
;                         for (int q = 0; q < 4; ++q) {
;                             const float r = sigmoidf_(ar[q] + vba[q]), ig = sigmoidf_(ain[q] + vbx[q]);
;                             const float la = -r * vsp[q];
;                             const float a = __expf(la);
;                             A[sg * 4 + q] = a; B[sg * 4 + q] = __builtin_amdgcn_sqrtf((1.f - a) * (1.f + a)) * (ig * xc[q]);
;                         }
;                     }
;     ...
;                     GATE_SCAN_STEP(1); GATE_SCAN_STEP(2); GATE_SCAN_STEP(4); GATE_SCAN_STEP(8);
.LBB0_587:
	s_or_b64 exec, exec, s[28:29]
	v_add_u32_e32 v82, 0xa0, v160
	v_ashrrev_i32_e32 v83, 31, v82
	v_lshlrev_b64 v[80:81], 10, v[82:83]
	v_lshl_add_u64 v[84:85], v[162:163], 0, v[80:81]
	v_add_f32_e32 v87, v72, v88
	v_add_u32_e32 v72, 0xb0, v160
	s_nop 0
	v_add_f32_e32 v105, v73, v89
	v_ashrrev_i32_e32 v73, 31, v72
	v_add_f32_e32 v86, v76, v92
	v_add_f32_e32 v104, v77, v93
	v_lshlrev_b64 v[76:77], 10, v[72:73]
	v_lshl_add_u64 v[84:85], v[162:163], 0, v[76:77]
	s_nop 0
	v_add_f32_e32 v78, v78, v94
	v_add_f32_e32 v79, v79, v95
	v_mul_f32_e32 v84, 0xbfb8aa3b, v86
	v_mul_f32_e32 v85, 0xbfb8aa3b, v87
	v_mul_f32_e32 v86, 0xbfb8aa3b, v104
	v_mul_f32_e32 v78, 0xbfb8aa3b, v78
	v_mul_f32_e32 v79, 0xbfb8aa3b, v79
	v_exp_f32_e32 v84, v84
	v_exp_f32_e32 v85, v85
	v_exp_f32_e32 v86, v86
	v_exp_f32_e32 v78, v78
	v_exp_f32_e32 v79, v79
	v_add_f32_e32 v68, v68, v92
	v_mul_f32_e32 v68, 0xbfb8aa3b, v68
	v_exp_f32_e32 v68, v68
	v_add_f32_e32 v84, 1.0, v84
	v_add_f32_e32 v85, 1.0, v85
	v_add_f32_e32 v86, 1.0, v86
	v_add_f32_e32 v78, 1.0, v78
	v_add_f32_e32 v79, 1.0, v79
	v_rcp_f32_e32 v84, v84
	v_rcp_f32_e32 v104, v85
	v_rcp_f32_e32 v85, v86
	v_rcp_f32_e32 v78, v78
	v_mul_f32_e32 v87, 0xbfb8aa3b, v105
	v_rcp_f32_e32 v79, v79
	v_exp_f32_e32 v87, v87
	v_add_f32_e32 v68, 1.0, v68
	v_add_f32_e32 v69, v69, v93
	v_rcp_f32_e32 v68, v68
	v_mul_f32_e32 v69, 0xbfb8aa3b, v69
	v_add_f32_e32 v74, v74, v90
	v_mul_f32_e32 v84, v96, v84
	v_mul_f32_e32 v85, v97, v85
	v_mul_f32_e32 v78, v98, v78
	v_exp_f32_e32 v69, v69
	v_add_f32_e32 v75, v75, v91
	v_mul_f32_e32 v74, 0xbfb8aa3b, v74
	v_mul_f32_e32 v79, v99, v79
	v_mul_f32_e32 v84, 0xbfb8aa3b, v84
	v_mul_f32_e32 v85, 0xbfb8aa3b, v85
	v_mul_f32_e32 v78, 0xbfb8aa3b, v78
	v_mul_f32_e32 v75, 0xbfb8aa3b, v75
	v_exp_f32_e32 v74, v74
	v_add_f32_e32 v87, 1.0, v87
	v_mul_f32_e32 v79, 0xbfb8aa3b, v79
	v_exp_f32_e32 v84, v84
	v_exp_f32_e32 v85, v85
	v_exp_f32_e32 v86, v78
	v_exp_f32_e32 v75, v75
	v_rcp_f32_e32 v105, v87
	v_exp_f32_e32 v87, v79
	v_add_f32_e32 v64, v64, v88
	v_mul_f32_e32 v68, v96, v68
	v_mul_f32_e32 v64, 0xbfb8aa3b, v64
	v_mul_f32_e32 v68, 0xbfb8aa3b, v68
	v_add_f32_e32 v69, 1.0, v69
	v_exp_f32_e32 v64, v64
	v_exp_f32_e32 v68, v68
	v_rcp_f32_e32 v69, v69
	v_add_f32_e32 v74, 1.0, v74
	v_sub_f32_e32 v78, 1.0, v84
	v_add_f32_e32 v79, 1.0, v84
	v_sub_f32_e32 v114, 1.0, v85
	v_add_f32_e32 v115, 1.0, v85
	v_sub_f32_e32 v118, 1.0, v86
	v_add_f32_e32 v119, 1.0, v86
	v_add_f32_e32 v75, 1.0, v75
	v_rcp_f32_e32 v74, v74
	v_sub_f32_e32 v120, 1.0, v87
	v_add_f32_e32 v121, 1.0, v87
	v_mul_f32_e32 v78, v78, v79
	v_mul_f32_e32 v79, v114, v115
	v_mul_f32_e32 v114, v118, v119
	v_rcp_f32_e32 v75, v75
	v_mul_f32_e32 v115, v120, v121
	v_sqrt_f32_e32 v78, v78
	v_sqrt_f32_e32 v79, v79
	v_sqrt_f32_e32 v114, v114
	v_sqrt_f32_e32 v115, v115
	v_add_f32_e32 v64, 1.0, v64
	v_sub_f32_e32 v88, 1.0, v68
	v_add_f32_e32 v92, 1.0, v68
	v_add_f32_e32 v65, v65, v89
	v_mul_f32_e32 v69, v97, v69
	s_waitcnt lgkmcnt(0)
	v_lshlrev_b32_e32 v118, 16, v216
	v_and_b32_e32 v102, 0xffff0000, v216
	v_lshlrev_b32_e32 v119, 16, v217
	v_rcp_f32_e32 v64, v64
	v_mul_f32_e32 v88, v88, v92
	v_mul_f32_e32 v65, 0xbfb8aa3b, v65
	v_mul_f32_e32 v69, 0xbfb8aa3b, v69
	v_add_f32_e32 v70, v70, v94
	v_and_b32_e32 v120, 0xffff0000, v217
	v_mul_f32_e32 v103, v104, v118
	v_mul_f32_e32 v104, v105, v102
	v_mul_f32_e32 v74, v74, v119
	v_sqrt_f32_e32 v88, v88
	v_exp_f32_e32 v65, v65
	v_exp_f32_e32 v69, v69
	v_mul_f32_e32 v70, 0xbfb8aa3b, v70
	v_mul_f32_e32 v102, v78, v103
	v_mul_f32_e32 v103, v79, v104
	v_mul_f32_e32 v104, v114, v74
	v_mul_f32_e32 v74, v75, v120
	v_exp_f32_e32 v70, v70
	v_mul_f32_e32 v105, v115, v74
	v_lshlrev_b32_e32 v74, 16, v218
	v_mul_f32_e32 v64, v64, v74
	v_mul_f32_e32 v74, v88, v64
	v_add_f32_e32 v64, 1.0, v65
	v_sub_f32_e32 v65, 1.0, v69
	v_add_f32_e32 v88, 1.0, v69
	v_rcp_f32_e32 v64, v64
	v_mul_f32_e32 v65, v65, v88
	v_add_f32_e32 v70, 1.0, v70
	v_sqrt_f32_e32 v65, v65
	v_rcp_f32_e32 v70, v70
	v_and_b32_e32 v75, 0xffff0000, v218
	v_mul_f32_e32 v64, v64, v75
	v_mul_f32_e32 v75, v65, v64
	v_mul_f32_e32 v65, v98, v70
	v_mul_f32_e32 v65, 0xbfb8aa3b, v65
	v_exp_f32_e32 v70, v65
	v_add_f32_e32 v65, v71, v95
	v_mul_f32_e32 v65, 0xbfb8aa3b, v65
	v_exp_f32_e32 v65, v65
	v_add_f32_e32 v66, v66, v90
	v_mul_f32_e32 v66, 0xbfb8aa3b, v66
	v_exp_f32_e32 v66, v66
	v_add_f32_e32 v65, 1.0, v65
	v_rcp_f32_e32 v65, v65
	v_add_f32_e32 v67, v67, v91
	v_add_f32_e32 v64, 1.0, v66
	v_sub_f32_e32 v66, 1.0, v70
	v_mul_f32_e32 v65, v99, v65
	v_add_f32_e32 v71, 1.0, v70
	v_mul_f32_e32 v67, 0xbfb8aa3b, v67
	v_mul_f32_e32 v65, 0xbfb8aa3b, v65
	v_mul_f32_e32 v66, v66, v71
	v_exp_f32_e32 v67, v67
	v_exp_f32_e32 v71, v65
	v_rcp_f32_e32 v64, v64
	v_sqrt_f32_e32 v65, v66
	v_add_f32_e32 v66, 1.0, v67
	v_sub_f32_e32 v67, 1.0, v71
	v_add_f32_e32 v88, 1.0, v71
	v_rcp_f32_e32 v66, v66
	v_mul_f32_e32 v67, v67, v88
	v_sqrt_f32_e32 v67, v67
	v_lshlrev_b32_e32 v78, 16, v219
	v_and_b32_e32 v79, 0xffff0000, v219
	v_mul_f32_e32 v64, v64, v78
	v_mul_f32_e32 v88, v65, v64
	v_mul_f32_e32 v64, v66, v79
	v_mul_f32_e32 v89, v67, v64
	s_nop 1
	v_fmac_f32_dpp v102, v102, v84 row_shr:1 row_mask:0xf bank_mask:0xf
	v_fmac_f32_dpp v103, v103, v85 row_shr:1 row_mask:0xf bank_mask:0xf
	v_fmac_f32_dpp v104, v104, v86 row_shr:1 row_mask:0xf bank_mask:0xf
	v_fmac_f32_dpp v105, v105, v87 row_shr:1 row_mask:0xf bank_mask:0xf
	v_fmac_f32_dpp v74, v74, v68 row_shr:1 row_mask:0xf bank_mask:0xf
	v_fmac_f32_dpp v75, v75, v69 row_shr:1 row_mask:0xf bank_mask:0xf
	v_fmac_f32_dpp v88, v88, v70 row_shr:1 row_mask:0xf bank_mask:0xf
	v_fmac_f32_dpp v89, v89, v71 row_shr:1 row_mask:0xf bank_mask:0xf
	v_mul_f32_dpp v84, v84, v84 row_shr:1 row_mask:0xf bank_mask:0xf
	v_mul_f32_dpp v85, v85, v85 row_shr:1 row_mask:0xf bank_mask:0xf
	v_mul_f32_dpp v86, v86, v86 row_shr:1 row_mask:0xf bank_mask:0xf
	v_mul_f32_dpp v87, v87, v87 row_shr:1 row_mask:0xf bank_mask:0xf
	v_mul_f32_dpp v68, v68, v68 row_shr:1 row_mask:0xf bank_mask:0xf
	v_mul_f32_dpp v69, v69, v69 row_shr:1 row_mask:0xf bank_mask:0xf
	v_mul_f32_dpp v70, v70, v70 row_shr:1 row_mask:0xf bank_mask:0xf
	v_mul_f32_dpp v71, v71, v71 row_shr:1 row_mask:0xf bank_mask:0xf

;     __device__ __forceinline__ void operator()(AccRef acc, const pg8::Unit& u, int wr, int wc, int fr, int fq) const {
;     ...
;                     GATE_SCAN_STEP(1); GATE_SCAN_STEP(2); GATE_SCAN_STEP(4); GATE_SCAN_STEP(8);
	v_lshlrev_b64 v[78:79], 9, v[82:83]
	s_nop 1
	v_fmac_f32_dpp v102, v102, v84 row_shr:2 row_mask:0xf bank_mask:0xf
	v_fmac_f32_dpp v103, v103, v85 row_shr:2 row_mask:0xf bank_mask:0xf
	v_fmac_f32_dpp v104, v104, v86 row_shr:2 row_mask:0xf bank_mask:0xf
	v_fmac_f32_dpp v105, v105, v87 row_shr:2 row_mask:0xf bank_mask:0xf
	v_fmac_f32_dpp v74, v74, v68 row_shr:2 row_mask:0xf bank_mask:0xf
	v_fmac_f32_dpp v75, v75, v69 row_shr:2 row_mask:0xf bank_mask:0xf
	v_fmac_f32_dpp v88, v88, v70 row_shr:2 row_mask:0xf bank_mask:0xf
	v_fmac_f32_dpp v89, v89, v71 row_shr:2 row_mask:0xf bank_mask:0xf
	v_mul_f32_dpp v84, v84, v84 row_shr:2 row_mask:0xf bank_mask:0xf
	v_mul_f32_dpp v85, v85, v85 row_shr:2 row_mask:0xf bank_mask:0xf
	v_mul_f32_dpp v86, v86, v86 row_shr:2 row_mask:0xf bank_mask:0xf
	v_mul_f32_dpp v87, v87, v87 row_shr:2 row_mask:0xf bank_mask:0xf
	v_mul_f32_dpp v68, v68, v68 row_shr:2 row_mask:0xf bank_mask:0xf
	v_mul_f32_dpp v69, v69, v69 row_shr:2 row_mask:0xf bank_mask:0xf
	v_mul_f32_dpp v70, v70, v70 row_shr:2 row_mask:0xf bank_mask:0xf
	v_mul_f32_dpp v71, v71, v71 row_shr:2 row_mask:0xf bank_mask:0xf

;     __device__ __forceinline__ void operator()(AccRef acc, const pg8::Unit& u, int wr, int wc, int fr, int fq) const {
;     ...
;                     GATE_SCAN_STEP(1); GATE_SCAN_STEP(2); GATE_SCAN_STEP(4); GATE_SCAN_STEP(8);
	v_lshl_add_u64 v[82:83], v[78:79], 0, v[152:153]
	s_nop 1
	v_fmac_f32_dpp v102, v102, v84 row_shr:4 row_mask:0xf bank_mask:0xf
	v_fmac_f32_dpp v103, v103, v85 row_shr:4 row_mask:0xf bank_mask:0xf
	v_fmac_f32_dpp v104, v104, v86 row_shr:4 row_mask:0xf bank_mask:0xf
	v_fmac_f32_dpp v105, v105, v87 row_shr:4 row_mask:0xf bank_mask:0xf
	v_fmac_f32_dpp v74, v74, v68 row_shr:4 row_mask:0xf bank_mask:0xf
	v_fmac_f32_dpp v75, v75, v69 row_shr:4 row_mask:0xf bank_mask:0xf
	v_fmac_f32_dpp v88, v88, v70 row_shr:4 row_mask:0xf bank_mask:0xf
	v_fmac_f32_dpp v89, v89, v71 row_shr:4 row_mask:0xf bank_mask:0xf
	v_mul_f32_dpp v84, v84, v84 row_shr:4 row_mask:0xf bank_mask:0xf
	v_mul_f32_dpp v85, v85, v85 row_shr:4 row_mask:0xf bank_mask:0xf
	v_mul_f32_dpp v86, v86, v86 row_shr:4 row_mask:0xf bank_mask:0xf
	v_mul_f32_dpp v87, v87, v87 row_shr:4 row_mask:0xf bank_mask:0xf
	v_mul_f32_dpp v68, v68, v68 row_shr:4 row_mask:0xf bank_mask:0xf
	v_mul_f32_dpp v69, v69, v69 row_shr:4 row_mask:0xf bank_mask:0xf
	v_mul_f32_dpp v70, v70, v70 row_shr:4 row_mask:0xf bank_mask:0xf
	v_mul_f32_dpp v71, v71, v71 row_shr:4 row_mask:0xf bank_mask:0xf

;     __device__ __forceinline__ void operator()(AccRef acc, const pg8::Unit& u, int wr, int wc, int fr, int fq) const {
;     ...
;                     GATE_SCAN_STEP(1); GATE_SCAN_STEP(2); GATE_SCAN_STEP(4); GATE_SCAN_STEP(8);
	v_lshlrev_b64 v[82:83], 2, v[82:83]
	s_nop 1
	v_fmac_f32_dpp v102, v102, v84 row_shr:8 row_mask:0xf bank_mask:0xf
	v_fmac_f32_dpp v103, v103, v85 row_shr:8 row_mask:0xf bank_mask:0xf
	v_fmac_f32_dpp v104, v104, v86 row_shr:8 row_mask:0xf bank_mask:0xf
	v_fmac_f32_dpp v105, v105, v87 row_shr:8 row_mask:0xf bank_mask:0xf
	v_fmac_f32_dpp v74, v74, v68 row_shr:8 row_mask:0xf bank_mask:0xf
	v_fmac_f32_dpp v75, v75, v69 row_shr:8 row_mask:0xf bank_mask:0xf
	v_fmac_f32_dpp v88, v88, v70 row_shr:8 row_mask:0xf bank_mask:0xf
	v_fmac_f32_dpp v89, v89, v71 row_shr:8 row_mask:0xf bank_mask:0xf
	v_mul_f32_dpp v84, v84, v84 row_shr:8 row_mask:0xf bank_mask:0xf
	v_mul_f32_dpp v85, v85, v85 row_shr:8 row_mask:0xf bank_mask:0xf
	v_mul_f32_dpp v86, v86, v86 row_shr:8 row_mask:0xf bank_mask:0xf
	v_mul_f32_dpp v87, v87, v87 row_shr:8 row_mask:0xf bank_mask:0xf
	v_mul_f32_dpp v68, v68, v68 row_shr:8 row_mask:0xf bank_mask:0xf
	v_mul_f32_dpp v69, v69, v69 row_shr:8 row_mask:0xf bank_mask:0xf
	v_mul_f32_dpp v70, v70, v70 row_shr:8 row_mask:0xf bank_mask:0xf
	v_mul_f32_dpp v71, v71, v71 row_shr:8 row_mask:0xf bank_mask:0xf

;     __device__ __forceinline__ void operator()(AccRef acc, const pg8::Unit& u, int wr, int wc, int fr, int fq) const {
;     ...
; #pragma unroll
;                     for (int q = 0; q < 4; ++q) {
;                         const float A1 = __int_as_float(__builtin_amdgcn_ds_bpermute(l15, __float_as_int(A[q]))), H1 = __int_as_float(__builtin_amdgcn_ds_bpermute(l15, __float_as_int(B[q])));
;                         B[4 + q] = fmaf(A[4 + q], H1, B[4 + q]); A[4 + q] *= A1; }
; #pragma unroll
;                     for (int sg = 0; sg < 2; ++sg) { const size_t ro = (size_t)(row0 + ai * 128 + (2 * mp + sg) * 16) * RW + ch;
;                         *(f32x4*)(SA + ro) = (f32x4){A[sg * 4], A[sg * 4 + 1], A[sg * 4 + 2], A[sg * 4 + 3]}; *(f32x4*)(SB + ro) = (f32x4){B[sg * 4], B[sg * 4 + 1], B[sg * 4 + 2], B[sg * 4 + 3]}; }
;                     if (fr == 15) { const size_t so = (size_t)(u.pm * 8 + ai * 4 + wr * 2 + mp) * RW + ch;
;                         *(f32x4*)(sumA + so) = (f32x4){A[4], A[5], A[6], A[7]}; *(f32x4*)(sumH + so) = (f32x4){B[4], B[5], B[6], B[7]}; }
	ds_bpermute_b32 v64, v168, v84
	ds_bpermute_b32 v90, v168, v102
	ds_bpermute_b32 v65, v168, v85
	ds_bpermute_b32 v91, v168, v103
	ds_bpermute_b32 v66, v168, v86
	ds_bpermute_b32 v92, v168, v104
	ds_bpermute_b32 v67, v168, v87
	ds_bpermute_b32 v93, v168, v105
	v_lshl_add_u64 v[94:95], s[6:7], 0, v[82:83]
	v_lshl_add_u64 v[82:83], s[8:9], 0, v[82:83]
	global_store_dwordx4 v[82:83], v[102:105], off
	v_lshlrev_b64 v[82:83], 9, v[72:73]
	v_lshl_add_u64 v[72:73], v[82:83], 0, v[152:153]
	v_lshlrev_b64 v[72:73], 2, v[72:73]
	global_store_dwordx4 v[94:95], v[84:87], off
	s_waitcnt lgkmcnt(0)
	v_pk_mul_f32 v[66:67], v[70:71], v[66:67]
	v_pk_mul_f32 v[64:65], v[68:69], v[64:65]
	v_lshl_add_u64 v[84:85], s[6:7], 0, v[72:73]
	v_pk_fma_f32 v[70:71], v[70:71], v[92:93], v[88:89]
	v_pk_fma_f32 v[68:69], v[68:69], v[90:91], v[74:75]
	v_lshl_add_u64 v[72:73], s[8:9], 0, v[72:73]
	global_store_dwordx4 v[84:85], v[64:67], off
	global_store_dwordx4 v[72:73], v[68:71], off
	s_and_saveexec_b64 s[28:29], s[0:1]
	s_cbranch_execz .LBB0_589
	s_lshl_b32 s56, s46, 3
	s_add_i32 s74, s56, s97
	s_ashr_i32 s75, s74, 31
	s_lshl_b64 s[74:75], s[74:75], 9
	v_lshl_add_u64 v[72:73], s[74:75], 0, v[152:153]
	v_lshlrev_b64 v[72:73], 2, v[72:73]
	v_lshl_add_u64 v[74:75], s[18:19], 0, v[72:73]
	global_store_dwordx4 v[74:75], v[64:67], off
	s_nop 1
	v_lshl_add_u64 v[64:65], s[20:21], 0, v[72:73]
	global_store_dwordx4 v[64:65], v[68:71], off
; __device__ __forceinline__ float bflo(unsigned w) { return __uint_as_float(w << 16); }
; __device__ __forceinline__ float bfhi(unsigned w) { return __uint_as_float(w & 0xffff0000u); }
; __device__ __forceinline__ float sigmoidf_(float x) { return __builtin_amdgcn_rcpf(1.f + __expf(-x)); }
;     __device__ __forceinline__ void operator()(AccRef acc, const pg8::Unit& u, int wr, int wc, int fr, int fq) const {
;     ...
;             const f32x4 vba = *(const f32x4*)(ba + ch), vbx = *(const f32x4*)(bx + ch), vsp = *(const f32x4*)(sp8 + ch);
; #pragma unroll
;             for (int ai = 0; ai < 2; ++ai)
; #pragma unroll
;                 for (int mp = 0; mp < 2; ++mp) {
;                     float A[8], B[8];
; #pragma unroll
;                     for (int sg = 0; sg < 2; ++sg) { const int m = 2 * mp + sg;
;                         const size_t ro = (size_t)(row0 + ai * 128 + m * 16) * RW + ch;
;                         const u32x2 xw = *(const u32x2*)(XC + ro);
;                         const float xc[4] = {bflo(xw.x), bfhi(xw.x), bflo(xw.y), bfhi(xw.y)};
;                         const f32x4 ar = acc[ai][0][m][n], ain = acc[ai][1][m][n];
; #pragma unroll
;                         for (int q = 0; q < 4; ++q) {
;                             const float r = sigmoidf_(ar[q] + vba[q]), ig = sigmoidf_(ain[q] + vbx[q]);
;                             const float la = -r * vsp[q];
;                             const float a = __expf(la);
;                             A[sg * 4 + q] = a; B[sg * 4 + q] = __builtin_amdgcn_sqrtf((1.f - a) * (1.f + a)) * (ig * xc[q]);
;                         }
;                     }
;     ...
;                     GATE_SCAN_STEP(1); GATE_SCAN_STEP(2); GATE_SCAN_STEP(4); GATE_SCAN_STEP(8);
.LBB0_589:
	s_or_b64 exec, exec, s[28:29]
	s_nop 0
	s_nop 0
	s_nop 0
	v_or_b32_e32 v84, 16, v152
	v_ashrrev_i32_e32 v85, 31, v84
	v_lshl_add_u64 v[88:89], s[10:11], 0, v[150:151]
	v_lshlrev_b64 v[86:87], 1, v[84:85]
	v_lshl_add_u64 v[88:89], v[88:89], 0, v[86:87]
	s_nop 0
	v_lshl_add_u64 v[96:97], v[132:133], 0, v[84:85]
	v_lshlrev_b64 v[96:97], 2, v[96:97]
	v_lshl_add_u64 v[98:99], s[6:7], 0, v[96:97]
	s_nop 0
	v_add_f32_e32 v60, v60, v242
	v_mul_f32_e32 v60, 0xbfb8aa3b, v60
	v_exp_f32_e32 v60, v60
	v_add_f32_e32 v61, v61, v243
	v_mul_f32_e32 v61, 0xbfb8aa3b, v61
	v_exp_f32_e32 v61, v61
	v_add_f32_e32 v60, 1.0, v60
	v_rcp_f32_e32 v60, v60
	v_add_f32_e32 v56, v56, v246
	v_mul_f32_e32 v56, 0xbfb8aa3b, v56
	v_add_f32_e32 v61, 1.0, v61
	s_waitcnt lgkmcnt(0)
	v_mul_f32_e32 v60, v250, v60
	v_mul_f32_e32 v60, 0xbfb8aa3b, v60
	v_add_f32_e32 v62, v62, v244
	v_exp_f32_e32 v56, v56
	v_exp_f32_e32 v60, v60
	v_rcp_f32_e32 v61, v61
	v_mul_f32_e32 v62, 0xbfb8aa3b, v62
	v_exp_f32_e32 v62, v62
	v_add_f32_e32 v56, 1.0, v56
	v_sub_f32_e32 v92, 1.0, v60
	v_add_f32_e32 v93, 1.0, v60
	v_add_f32_e32 v57, v57, v247
	v_mul_f32_e32 v61, v251, v61
	v_rcp_f32_e32 v56, v56
	v_mul_f32_e32 v92, v92, v93
	v_mul_f32_e32 v57, 0xbfb8aa3b, v57
	v_mul_f32_e32 v61, 0xbfb8aa3b, v61
	v_add_f32_e32 v62, 1.0, v62
	v_add_f32_e32 v63, v63, v245
	v_sqrt_f32_e32 v92, v92
	v_exp_f32_e32 v57, v57
	v_exp_f32_e32 v61, v61
	v_rcp_f32_e32 v62, v62
	v_mul_f32_e32 v63, 0xbfb8aa3b, v63
	v_exp_f32_e32 v63, v63
	v_lshlrev_b32_e32 v90, 16, v220
	v_mul_f32_e32 v56, v56, v90
	v_mul_f32_e32 v56, v56, v92
	v_add_f32_e32 v57, 1.0, v57
	v_sub_f32_e32 v90, 1.0, v61
	v_add_f32_e32 v92, 1.0, v61
	v_add_f32_e32 v58, v58, v248
	v_mul_f32_e32 v62, v252, v62
	v_rcp_f32_e32 v57, v57
	v_mul_f32_e32 v90, v90, v92
	v_mul_f32_e32 v58, 0xbfb8aa3b, v58
	v_mul_f32_e32 v62, 0xbfb8aa3b, v62
	v_add_f32_e32 v63, 1.0, v63
	v_sqrt_f32_e32 v90, v90
	v_exp_f32_e32 v58, v58
	v_exp_f32_e32 v62, v62
	v_rcp_f32_e32 v63, v63
	v_and_b32_e32 v88, 0xffff0000, v220
	v_mul_f32_e32 v57, v57, v88
	v_mul_f32_e32 v57, v57, v90
	v_add_f32_e32 v58, 1.0, v58
	v_sub_f32_e32 v88, 1.0, v62
	v_add_f32_e32 v90, 1.0, v62
	v_add_f32_e32 v59, v59, v249
	v_mul_f32_e32 v63, v253, v63
	v_rcp_f32_e32 v58, v58
	v_mul_f32_e32 v88, v88, v90
	v_mul_f32_e32 v59, 0xbfb8aa3b, v59
	v_mul_f32_e32 v63, 0xbfb8aa3b, v63
	v_sqrt_f32_e32 v88, v88
	v_exp_f32_e32 v59, v59
	v_exp_f32_e32 v63, v63
	v_lshlrev_b32_e32 v91, 16, v221
	v_mul_f32_e32 v58, v58, v91
	v_mul_f32_e32 v58, v58, v88
	v_add_f32_e32 v59, 1.0, v59
	v_sub_f32_e32 v88, 1.0, v63
	v_add_f32_e32 v90, 1.0, v63
	v_rcp_f32_e32 v59, v59
	v_mul_f32_e32 v88, v88, v90
	v_sqrt_f32_e32 v88, v88
	v_and_b32_e32 v89, 0xffff0000, v221
	v_mul_f32_e32 v59, v59, v89
	v_add_f32_e32 v52, v52, v242
	v_mul_f32_e32 v59, v59, v88
	v_lshl_add_u64 v[88:89], s[10:11], 0, v[148:149]
	v_lshl_add_u64 v[88:89], v[88:89], 0, v[86:87]
	s_nop 0
	v_mul_f32_e32 v52, 0xbfb8aa3b, v52
	v_exp_f32_e32 v52, v52
	v_add_f32_e32 v48, v48, v246
	v_mul_f32_e32 v48, 0xbfb8aa3b, v48
	v_exp_f32_e32 v48, v48
	v_add_f32_e32 v52, 1.0, v52
	v_rcp_f32_e32 v52, v52
	v_add_f32_e32 v49, v49, v247
	v_add_f32_e32 v48, 1.0, v48
	v_rcp_f32_e32 v48, v48
	v_mul_f32_e32 v52, v250, v52
	v_mul_f32_e32 v52, 0xbfb8aa3b, v52
	v_exp_f32_e32 v52, v52
	v_mul_f32_e32 v49, 0xbfb8aa3b, v49
	v_exp_f32_e32 v49, v49
	s_waitcnt lgkmcnt(0)
	v_lshlrev_b32_e32 v92, 16, v222
	v_and_b32_e32 v93, 0xffff0000, v222
	v_lshlrev_b32_e32 v91, 16, v223
	v_and_b32_e32 v90, 0xffff0000, v223
	v_sub_f32_e32 v88, 1.0, v52
	v_add_f32_e32 v89, 1.0, v52
	v_mul_f32_e32 v88, v88, v89
	v_sqrt_f32_e32 v88, v88
	v_mul_f32_e32 v48, v48, v92
	v_add_f32_e32 v49, 1.0, v49
	v_rcp_f32_e32 v49, v49
	v_mul_f32_e32 v88, v48, v88
	v_add_f32_e32 v48, v53, v243
	v_mul_f32_e32 v48, 0xbfb8aa3b, v48
	v_exp_f32_e32 v48, v48
	v_mul_f32_e32 v49, v49, v93
	v_add_f32_e32 v48, 1.0, v48
	v_rcp_f32_e32 v48, v48
	s_nop 0
	v_mul_f32_e32 v48, v251, v48
	v_mul_f32_e32 v48, 0xbfb8aa3b, v48
	v_exp_f32_e32 v53, v48
	s_nop 0
	v_sub_f32_e32 v48, 1.0, v53
	v_add_f32_e32 v89, 1.0, v53
	v_mul_f32_e32 v48, v48, v89
	v_sqrt_f32_e32 v48, v48
	s_nop 0
	v_mul_f32_e32 v89, v49, v48
	v_add_f32_e32 v48, v54, v244
	v_mul_f32_e32 v48, 0xbfb8aa3b, v48
	v_exp_f32_e32 v48, v48
	v_add_f32_e32 v49, v50, v248
	v_mul_f32_e32 v49, 0xbfb8aa3b, v49
	v_exp_f32_e32 v49, v49
	v_add_f32_e32 v48, 1.0, v48
	v_rcp_f32_e32 v48, v48
	v_add_f32_e32 v49, 1.0, v49
	v_rcp_f32_e32 v49, v49
	v_mul_f32_e32 v48, v252, v48
	v_mul_f32_e32 v48, 0xbfb8aa3b, v48
	v_exp_f32_e32 v54, v48
	v_mul_f32_e32 v49, v49, v91
	v_sub_f32_e32 v48, 1.0, v54
	v_add_f32_e32 v50, 1.0, v54
	v_mul_f32_e32 v48, v48, v50
	v_sqrt_f32_e32 v48, v48
	s_nop 0
	v_mul_f32_e32 v92, v49, v48
	v_add_f32_e32 v48, v55, v245
	v_mul_f32_e32 v48, 0xbfb8aa3b, v48
	v_exp_f32_e32 v48, v48
	v_add_f32_e32 v49, v51, v249
	v_mul_f32_e32 v49, 0xbfb8aa3b, v49
	v_exp_f32_e32 v49, v49
	v_add_f32_e32 v48, 1.0, v48
	v_rcp_f32_e32 v48, v48
	v_add_f32_e32 v49, 1.0, v49
	v_rcp_f32_e32 v49, v49
	v_mul_f32_e32 v48, v253, v48
	v_mul_f32_e32 v48, 0xbfb8aa3b, v48
	v_exp_f32_e32 v55, v48
	v_mul_f32_e32 v49, v49, v90
	v_sub_f32_e32 v48, 1.0, v55
	v_add_f32_e32 v50, 1.0, v55
	v_mul_f32_e32 v48, v48, v50
	v_sqrt_f32_e32 v48, v48
	s_nop 0
	v_mul_f32_e32 v93, v49, v48
	s_nop 1
	v_fmac_f32_dpp v56, v56, v60 row_shr:1 row_mask:0xf bank_mask:0xf
	v_fmac_f32_dpp v57, v57, v61 row_shr:1 row_mask:0xf bank_mask:0xf
	v_fmac_f32_dpp v58, v58, v62 row_shr:1 row_mask:0xf bank_mask:0xf
	v_fmac_f32_dpp v59, v59, v63 row_shr:1 row_mask:0xf bank_mask:0xf
	v_fmac_f32_dpp v88, v88, v52 row_shr:1 row_mask:0xf bank_mask:0xf
	v_fmac_f32_dpp v89, v89, v53 row_shr:1 row_mask:0xf bank_mask:0xf
	v_fmac_f32_dpp v92, v92, v54 row_shr:1 row_mask:0xf bank_mask:0xf
	v_fmac_f32_dpp v93, v93, v55 row_shr:1 row_mask:0xf bank_mask:0xf
	v_mul_f32_dpp v60, v60, v60 row_shr:1 row_mask:0xf bank_mask:0xf
	v_mul_f32_dpp v61, v61, v61 row_shr:1 row_mask:0xf bank_mask:0xf
	v_mul_f32_dpp v62, v62, v62 row_shr:1 row_mask:0xf bank_mask:0xf
	v_mul_f32_dpp v63, v63, v63 row_shr:1 row_mask:0xf bank_mask:0xf
	v_mul_f32_dpp v52, v52, v52 row_shr:1 row_mask:0xf bank_mask:0xf
	v_mul_f32_dpp v53, v53, v53 row_shr:1 row_mask:0xf bank_mask:0xf
	v_mul_f32_dpp v54, v54, v54 row_shr:1 row_mask:0xf bank_mask:0xf
	v_mul_f32_dpp v55, v55, v55 row_shr:1 row_mask:0xf bank_mask:0xf

;     __device__ __forceinline__ void operator()(AccRef acc, const pg8::Unit& u, int wr, int wc, int fr, int fq) const {
;     ...
;                     GATE_SCAN_STEP(1); GATE_SCAN_STEP(2); GATE_SCAN_STEP(4); GATE_SCAN_STEP(8);
	s_nop 0
	s_nop 1
	v_fmac_f32_dpp v56, v56, v60 row_shr:2 row_mask:0xf bank_mask:0xf
	v_fmac_f32_dpp v57, v57, v61 row_shr:2 row_mask:0xf bank_mask:0xf
	v_fmac_f32_dpp v58, v58, v62 row_shr:2 row_mask:0xf bank_mask:0xf
	v_fmac_f32_dpp v59, v59, v63 row_shr:2 row_mask:0xf bank_mask:0xf
	v_fmac_f32_dpp v88, v88, v52 row_shr:2 row_mask:0xf bank_mask:0xf
	v_fmac_f32_dpp v89, v89, v53 row_shr:2 row_mask:0xf bank_mask:0xf
	v_fmac_f32_dpp v92, v92, v54 row_shr:2 row_mask:0xf bank_mask:0xf
	v_fmac_f32_dpp v93, v93, v55 row_shr:2 row_mask:0xf bank_mask:0xf
	v_mul_f32_dpp v60, v60, v60 row_shr:2 row_mask:0xf bank_mask:0xf
	v_mul_f32_dpp v61, v61, v61 row_shr:2 row_mask:0xf bank_mask:0xf
	v_mul_f32_dpp v62, v62, v62 row_shr:2 row_mask:0xf bank_mask:0xf
	v_mul_f32_dpp v63, v63, v63 row_shr:2 row_mask:0xf bank_mask:0xf
	v_mul_f32_dpp v52, v52, v52 row_shr:2 row_mask:0xf bank_mask:0xf
	v_mul_f32_dpp v53, v53, v53 row_shr:2 row_mask:0xf bank_mask:0xf
	v_mul_f32_dpp v54, v54, v54 row_shr:2 row_mask:0xf bank_mask:0xf
	v_mul_f32_dpp v55, v55, v55 row_shr:2 row_mask:0xf bank_mask:0xf

;     __device__ __forceinline__ void operator()(AccRef acc, const pg8::Unit& u, int wr, int wc, int fr, int fq) const {
;     ...
;                     GATE_SCAN_STEP(1); GATE_SCAN_STEP(2); GATE_SCAN_STEP(4); GATE_SCAN_STEP(8);
	s_nop 0
	s_nop 1
	v_fmac_f32_dpp v56, v56, v60 row_shr:4 row_mask:0xf bank_mask:0xf
	v_fmac_f32_dpp v57, v57, v61 row_shr:4 row_mask:0xf bank_mask:0xf
	v_fmac_f32_dpp v58, v58, v62 row_shr:4 row_mask:0xf bank_mask:0xf
	v_fmac_f32_dpp v59, v59, v63 row_shr:4 row_mask:0xf bank_mask:0xf
	v_fmac_f32_dpp v88, v88, v52 row_shr:4 row_mask:0xf bank_mask:0xf
	v_fmac_f32_dpp v89, v89, v53 row_shr:4 row_mask:0xf bank_mask:0xf
	v_fmac_f32_dpp v92, v92, v54 row_shr:4 row_mask:0xf bank_mask:0xf
	v_fmac_f32_dpp v93, v93, v55 row_shr:4 row_mask:0xf bank_mask:0xf
	v_mul_f32_dpp v60, v60, v60 row_shr:4 row_mask:0xf bank_mask:0xf
	v_mul_f32_dpp v61, v61, v61 row_shr:4 row_mask:0xf bank_mask:0xf
	v_mul_f32_dpp v62, v62, v62 row_shr:4 row_mask:0xf bank_mask:0xf
	v_mul_f32_dpp v63, v63, v63 row_shr:4 row_mask:0xf bank_mask:0xf
	v_mul_f32_dpp v52, v52, v52 row_shr:4 row_mask:0xf bank_mask:0xf
	v_mul_f32_dpp v53, v53, v53 row_shr:4 row_mask:0xf bank_mask:0xf
	v_mul_f32_dpp v54, v54, v54 row_shr:4 row_mask:0xf bank_mask:0xf
	v_mul_f32_dpp v55, v55, v55 row_shr:4 row_mask:0xf bank_mask:0xf

;     __device__ __forceinline__ void operator()(AccRef acc, const pg8::Unit& u, int wr, int wc, int fr, int fq) const {
;     ...
;                     GATE_SCAN_STEP(1); GATE_SCAN_STEP(2); GATE_SCAN_STEP(4); GATE_SCAN_STEP(8);
	s_nop 0
	s_nop 1
	v_fmac_f32_dpp v56, v56, v60 row_shr:8 row_mask:0xf bank_mask:0xf
	v_fmac_f32_dpp v57, v57, v61 row_shr:8 row_mask:0xf bank_mask:0xf
	v_fmac_f32_dpp v58, v58, v62 row_shr:8 row_mask:0xf bank_mask:0xf
	v_fmac_f32_dpp v59, v59, v63 row_shr:8 row_mask:0xf bank_mask:0xf
	v_fmac_f32_dpp v88, v88, v52 row_shr:8 row_mask:0xf bank_mask:0xf
	v_fmac_f32_dpp v89, v89, v53 row_shr:8 row_mask:0xf bank_mask:0xf
	v_fmac_f32_dpp v92, v92, v54 row_shr:8 row_mask:0xf bank_mask:0xf
	v_fmac_f32_dpp v93, v93, v55 row_shr:8 row_mask:0xf bank_mask:0xf
	v_mul_f32_dpp v60, v60, v60 row_shr:8 row_mask:0xf bank_mask:0xf
	v_mul_f32_dpp v61, v61, v61 row_shr:8 row_mask:0xf bank_mask:0xf
	v_mul_f32_dpp v62, v62, v62 row_shr:8 row_mask:0xf bank_mask:0xf
	v_mul_f32_dpp v63, v63, v63 row_shr:8 row_mask:0xf bank_mask:0xf
	v_mul_f32_dpp v52, v52, v52 row_shr:8 row_mask:0xf bank_mask:0xf
	v_mul_f32_dpp v53, v53, v53 row_shr:8 row_mask:0xf bank_mask:0xf
	v_mul_f32_dpp v54, v54, v54 row_shr:8 row_mask:0xf bank_mask:0xf
	v_mul_f32_dpp v55, v55, v55 row_shr:8 row_mask:0xf bank_mask:0xf

;     __device__ __forceinline__ void operator()(AccRef acc, const pg8::Unit& u, int wr, int wc, int fr, int fq) const {
;     ...
; #pragma unroll
;                     for (int q = 0; q < 4; ++q) {
;                         const float A1 = __int_as_float(__builtin_amdgcn_ds_bpermute(l15, __float_as_int(A[q]))), H1 = __int_as_float(__builtin_amdgcn_ds_bpermute(l15, __float_as_int(B[q])));
;                         B[4 + q] = fmaf(A[4 + q], H1, B[4 + q]); A[4 + q] *= A1; }
; #pragma unroll
;                     for (int sg = 0; sg < 2; ++sg) { const size_t ro = (size_t)(row0 + ai * 128 + (2 * mp + sg) * 16) * RW + ch;
;                         *(f32x4*)(SA + ro) = (f32x4){A[sg * 4], A[sg * 4 + 1], A[sg * 4 + 2], A[sg * 4 + 3]}; *(f32x4*)(SB + ro) = (f32x4){B[sg * 4], B[sg * 4 + 1], B[sg * 4 + 2], B[sg * 4 + 3]}; }
;                     if (fr == 15) { const size_t so = (size_t)(u.pm * 8 + ai * 4 + wr * 2 + mp) * RW + ch;
;                         *(f32x4*)(sumA + so) = (f32x4){A[4], A[5], A[6], A[7]}; *(f32x4*)(sumH + so) = (f32x4){B[4], B[5], B[6], B[7]}; }
	ds_bpermute_b32 v48, v168, v60
	ds_bpermute_b32 v90, v168, v56
	ds_bpermute_b32 v49, v168, v61
	ds_bpermute_b32 v91, v168, v57
	ds_bpermute_b32 v50, v168, v62
	ds_bpermute_b32 v94, v168, v58
	ds_bpermute_b32 v51, v168, v63
	ds_bpermute_b32 v95, v168, v59
	global_store_dwordx4 v[98:99], v[60:63], off
	s_waitcnt lgkmcnt(0)
	v_pk_mul_f32 v[48:49], v[52:53], v[48:49]
	v_pk_fma_f32 v[52:53], v[52:53], v[90:91], v[88:89]
	v_lshl_add_u64 v[60:61], s[8:9], 0, v[96:97]
	global_store_dwordx4 v[60:61], v[56:59], off
	v_pk_mul_f32 v[50:51], v[54:55], v[50:51]
	v_pk_fma_f32 v[54:55], v[54:55], v[94:95], v[92:93]
	v_lshl_add_u64 v[56:57], v[134:135], 0, v[84:85]
	v_lshlrev_b64 v[56:57], 2, v[56:57]
	v_lshl_add_u64 v[58:59], s[6:7], 0, v[56:57]
	v_lshl_add_u64 v[56:57], s[8:9], 0, v[56:57]
	global_store_dwordx4 v[58:59], v[48:51], off
	global_store_dwordx4 v[56:57], v[52:55], off
	s_and_saveexec_b64 s[28:29], s[0:1]
	s_cbranch_execz .LBB0_591
	s_lshl_b32 s56, s46, 3
	s_add_i32 s74, s56, s94
	s_ashr_i32 s75, s74, 31
	s_lshl_b64 s[74:75], s[74:75], 9
	v_lshl_add_u64 v[56:57], s[74:75], 0, v[84:85]
	v_lshlrev_b64 v[56:57], 2, v[56:57]
	v_lshl_add_u64 v[58:59], s[18:19], 0, v[56:57]
	global_store_dwordx4 v[58:59], v[48:51], off
	s_nop 1
	v_lshl_add_u64 v[48:49], s[20:21], 0, v[56:57]
	global_store_dwordx4 v[48:49], v[52:55], off
; __device__ __forceinline__ float bflo(unsigned w) { return __uint_as_float(w << 16); }
; __device__ __forceinline__ float bfhi(unsigned w) { return __uint_as_float(w & 0xffff0000u); }
; __device__ __forceinline__ float sigmoidf_(float x) { return __builtin_amdgcn_rcpf(1.f + __expf(-x)); }
;     __device__ __forceinline__ void operator()(AccRef acc, const pg8::Unit& u, int wr, int wc, int fr, int fq) const {
;     ...
;                 for (int mp = 0; mp < 2; ++mp) {
;                     float A[8], B[8];
; #pragma unroll
;                     for (int sg = 0; sg < 2; ++sg) { const int m = 2 * mp + sg;
;                         const size_t ro = (size_t)(row0 + ai * 128 + m * 16) * RW + ch;
;                         const u32x2 xw = *(const u32x2*)(XC + ro);
;                         const float xc[4] = {bflo(xw.x), bfhi(xw.x), bflo(xw.y), bfhi(xw.y)};
;                         const f32x4 ar = acc[ai][0][m][n], ain = acc[ai][1][m][n];
; #pragma unroll
;                         for (int q = 0; q < 4; ++q) {
;                             const float r = sigmoidf_(ar[q] + vba[q]), ig = sigmoidf_(ain[q] + vbx[q]);
;                             const float la = -r * vsp[q];
;                             const float a = __expf(la);
;                             A[sg * 4 + q] = a; B[sg * 4 + q] = __builtin_amdgcn_sqrtf((1.f - a) * (1.f + a)) * (ig * xc[q]);
;                         }
;                     }
;     ...
;                     GATE_SCAN_STEP(1); GATE_SCAN_STEP(2); GATE_SCAN_STEP(4); GATE_SCAN_STEP(8);
.LBB0_591:
	s_or_b64 exec, exec, s[28:29]
	v_lshl_add_u64 v[48:49], s[10:11], 0, v[124:125]
	v_lshl_add_u64 v[48:49], v[48:49], 0, v[86:87]
	s_nop 0
	v_add_f32_e32 v44, v44, v242
	v_mul_f32_e32 v44, 0xbfb8aa3b, v44
	v_exp_f32_e32 v44, v44
	v_add_f32_e32 v45, v45, v243
	v_mul_f32_e32 v45, 0xbfb8aa3b, v45
	v_exp_f32_e32 v45, v45
	v_add_f32_e32 v44, 1.0, v44
	v_rcp_f32_e32 v44, v44
	v_add_f32_e32 v40, v40, v246
	v_mul_f32_e32 v40, 0xbfb8aa3b, v40
	v_add_f32_e32 v45, 1.0, v45
	v_mul_f32_e32 v44, v250, v44
	v_mul_f32_e32 v44, 0xbfb8aa3b, v44
	v_add_f32_e32 v46, v46, v244
	v_exp_f32_e32 v40, v40
	v_exp_f32_e32 v44, v44
	v_rcp_f32_e32 v45, v45
	v_mul_f32_e32 v46, 0xbfb8aa3b, v46
	v_exp_f32_e32 v46, v46
	v_add_f32_e32 v40, 1.0, v40
	v_sub_f32_e32 v52, 1.0, v44
	v_add_f32_e32 v53, 1.0, v44
	v_add_f32_e32 v41, v41, v247
	v_mul_f32_e32 v45, v251, v45
	v_rcp_f32_e32 v40, v40
	v_mul_f32_e32 v52, v52, v53
	v_mul_f32_e32 v41, 0xbfb8aa3b, v41
	v_mul_f32_e32 v45, 0xbfb8aa3b, v45
	v_add_f32_e32 v46, 1.0, v46
	v_add_f32_e32 v47, v47, v245
	v_sqrt_f32_e32 v52, v52
	v_exp_f32_e32 v41, v41
	v_exp_f32_e32 v45, v45
	v_rcp_f32_e32 v46, v46
	v_mul_f32_e32 v47, 0xbfb8aa3b, v47
	v_exp_f32_e32 v47, v47
	v_add_f32_e32 v41, 1.0, v41
	v_add_f32_e32 v42, v42, v248
	v_mul_f32_e32 v46, v252, v46
	v_rcp_f32_e32 v41, v41
	v_mul_f32_e32 v42, 0xbfb8aa3b, v42
	v_mul_f32_e32 v46, 0xbfb8aa3b, v46
	v_add_f32_e32 v47, 1.0, v47
	v_exp_f32_e32 v42, v42
	v_exp_f32_e32 v46, v46
	v_rcp_f32_e32 v47, v47
	v_add_f32_e32 v43, v43, v249
	v_add_f32_e32 v42, 1.0, v42
	v_rcp_f32_e32 v42, v42
	v_mul_f32_e32 v47, v253, v47
	v_mul_f32_e32 v43, 0xbfb8aa3b, v43
	v_mul_f32_e32 v47, 0xbfb8aa3b, v47
	v_exp_f32_e32 v43, v43
	v_exp_f32_e32 v47, v47
	v_add_f32_e32 v36, v36, v242
	v_mul_f32_e32 v36, 0xbfb8aa3b, v36
	v_add_f32_e32 v43, 1.0, v43
	v_rcp_f32_e32 v43, v43
	v_exp_f32_e32 v36, v36
	v_add_f32_e32 v32, v32, v246
	v_mul_f32_e32 v32, 0xbfb8aa3b, v32
	v_exp_f32_e32 v32, v32
	v_add_f32_e32 v36, 1.0, v36
	v_rcp_f32_e32 v36, v36
	v_add_f32_e32 v33, v33, v247
	v_add_f32_e32 v32, 1.0, v32
	v_rcp_f32_e32 v32, v32
	v_mul_f32_e32 v36, v250, v36
	v_mul_f32_e32 v36, 0xbfb8aa3b, v36
	v_exp_f32_e32 v36, v36
	v_mul_f32_e32 v33, 0xbfb8aa3b, v33
	v_exp_f32_e32 v33, v33
	v_lshl_add_u64 v[56:57], v[128:129], 0, v[84:85]
	v_lshlrev_b64 v[56:57], 2, v[56:57]
	v_lshl_add_u64 v[58:59], s[6:7], 0, v[56:57]
	v_add_f32_e32 v33, 1.0, v33
	v_rcp_f32_e32 v33, v33
	s_waitcnt lgkmcnt(0)
	v_lshlrev_b32_e32 v50, 16, v224
	v_mul_f32_e32 v40, v40, v50
	v_mul_f32_e32 v40, v52, v40
	v_sub_f32_e32 v50, 1.0, v45
	v_add_f32_e32 v52, 1.0, v45
	v_mul_f32_e32 v50, v50, v52
	v_sqrt_f32_e32 v50, v50
	v_and_b32_e32 v48, 0xffff0000, v224
	v_mul_f32_e32 v41, v41, v48
	v_sub_f32_e32 v48, 1.0, v46
	v_mul_f32_e32 v41, v50, v41
	v_add_f32_e32 v50, 1.0, v46
	v_mul_f32_e32 v48, v48, v50
	v_sqrt_f32_e32 v48, v48
	v_lshlrev_b32_e32 v51, 16, v225
	v_mul_f32_e32 v42, v42, v51
	v_add_f32_e32 v50, 1.0, v47
	v_mul_f32_e32 v42, v48, v42
	v_sub_f32_e32 v48, 1.0, v47
	v_mul_f32_e32 v48, v48, v50
	v_sqrt_f32_e32 v48, v48
	v_and_b32_e32 v49, 0xffff0000, v225
	v_mul_f32_e32 v43, v43, v49
	v_mul_f32_e32 v43, v48, v43
	v_lshl_add_u64 v[48:49], s[10:11], 0, v[126:127]
	v_lshl_add_u64 v[48:49], v[48:49], 0, v[86:87]
	s_nop 0
	s_waitcnt lgkmcnt(0)
	v_lshlrev_b32_e32 v51, 16, v226
	v_and_b32_e32 v52, 0xffff0000, v226
	v_lshlrev_b32_e32 v53, 16, v227
	v_and_b32_e32 v50, 0xffff0000, v227
	v_sub_f32_e32 v48, 1.0, v36
	v_add_f32_e32 v49, 1.0, v36
	v_mul_f32_e32 v48, v48, v49
	v_sqrt_f32_e32 v48, v48
	v_mul_f32_e32 v32, v32, v51
	v_mul_f32_e32 v33, v33, v52
	v_mul_f32_e32 v48, v48, v32
	v_add_f32_e32 v32, v37, v243
	v_mul_f32_e32 v32, 0xbfb8aa3b, v32
	v_exp_f32_e32 v32, v32
	s_nop 0
	v_add_f32_e32 v32, 1.0, v32
	v_rcp_f32_e32 v32, v32
	s_nop 0
	v_mul_f32_e32 v32, v251, v32
	v_mul_f32_e32 v32, 0xbfb8aa3b, v32
	v_exp_f32_e32 v37, v32
	s_nop 0
	v_sub_f32_e32 v32, 1.0, v37
	v_add_f32_e32 v49, 1.0, v37
	v_mul_f32_e32 v32, v32, v49
	v_sqrt_f32_e32 v32, v32
	s_nop 0
	v_mul_f32_e32 v49, v32, v33
	v_add_f32_e32 v32, v38, v244
	v_mul_f32_e32 v32, 0xbfb8aa3b, v32
	v_exp_f32_e32 v32, v32
	v_add_f32_e32 v33, v34, v248
	v_mul_f32_e32 v33, 0xbfb8aa3b, v33
	v_exp_f32_e32 v33, v33
	v_add_f32_e32 v32, 1.0, v32
	v_rcp_f32_e32 v32, v32
	v_add_f32_e32 v33, 1.0, v33
	v_rcp_f32_e32 v33, v33
	v_mul_f32_e32 v32, v252, v32
	v_mul_f32_e32 v32, 0xbfb8aa3b, v32
	v_exp_f32_e32 v38, v32
	v_mul_f32_e32 v33, v33, v53
	v_sub_f32_e32 v32, 1.0, v38
	v_add_f32_e32 v34, 1.0, v38
	v_mul_f32_e32 v32, v32, v34
	v_sqrt_f32_e32 v32, v32
	s_nop 0
	v_mul_f32_e32 v52, v32, v33
	v_add_f32_e32 v32, v39, v245
	v_mul_f32_e32 v32, 0xbfb8aa3b, v32
	v_exp_f32_e32 v32, v32
	v_add_f32_e32 v33, v35, v249
	v_mul_f32_e32 v33, 0xbfb8aa3b, v33
	v_exp_f32_e32 v33, v33
	v_add_f32_e32 v32, 1.0, v32
	v_rcp_f32_e32 v32, v32
	v_add_f32_e32 v33, 1.0, v33
	v_rcp_f32_e32 v33, v33
	v_mul_f32_e32 v32, v253, v32
	v_mul_f32_e32 v32, 0xbfb8aa3b, v32
	v_exp_f32_e32 v39, v32
	v_mul_f32_e32 v33, v33, v50
	v_sub_f32_e32 v32, 1.0, v39
	v_add_f32_e32 v34, 1.0, v39
	v_mul_f32_e32 v32, v32, v34
	v_sqrt_f32_e32 v32, v32
	s_nop 0
	v_mul_f32_e32 v53, v32, v33
	s_nop 1
	v_fmac_f32_dpp v40, v40, v44 row_shr:1 row_mask:0xf bank_mask:0xf
	v_fmac_f32_dpp v41, v41, v45 row_shr:1 row_mask:0xf bank_mask:0xf
	v_fmac_f32_dpp v42, v42, v46 row_shr:1 row_mask:0xf bank_mask:0xf
	v_fmac_f32_dpp v43, v43, v47 row_shr:1 row_mask:0xf bank_mask:0xf
	v_fmac_f32_dpp v48, v48, v36 row_shr:1 row_mask:0xf bank_mask:0xf
	v_fmac_f32_dpp v49, v49, v37 row_shr:1 row_mask:0xf bank_mask:0xf
	v_fmac_f32_dpp v52, v52, v38 row_shr:1 row_mask:0xf bank_mask:0xf
	v_fmac_f32_dpp v53, v53, v39 row_shr:1 row_mask:0xf bank_mask:0xf
	v_mul_f32_dpp v44, v44, v44 row_shr:1 row_mask:0xf bank_mask:0xf
	v_mul_f32_dpp v45, v45, v45 row_shr:1 row_mask:0xf bank_mask:0xf
	v_mul_f32_dpp v46, v46, v46 row_shr:1 row_mask:0xf bank_mask:0xf
	v_mul_f32_dpp v47, v47, v47 row_shr:1 row_mask:0xf bank_mask:0xf
	v_mul_f32_dpp v36, v36, v36 row_shr:1 row_mask:0xf bank_mask:0xf
	v_mul_f32_dpp v37, v37, v37 row_shr:1 row_mask:0xf bank_mask:0xf
	v_mul_f32_dpp v38, v38, v38 row_shr:1 row_mask:0xf bank_mask:0xf
	v_mul_f32_dpp v39, v39, v39 row_shr:1 row_mask:0xf bank_mask:0xf

;     __device__ __forceinline__ void operator()(AccRef acc, const pg8::Unit& u, int wr, int wc, int fr, int fq) const {
;     ...
;                     GATE_SCAN_STEP(1); GATE_SCAN_STEP(2); GATE_SCAN_STEP(4); GATE_SCAN_STEP(8);
	s_nop 0
	s_nop 1
	v_fmac_f32_dpp v40, v40, v44 row_shr:2 row_mask:0xf bank_mask:0xf
	v_fmac_f32_dpp v41, v41, v45 row_shr:2 row_mask:0xf bank_mask:0xf
	v_fmac_f32_dpp v42, v42, v46 row_shr:2 row_mask:0xf bank_mask:0xf
	v_fmac_f32_dpp v43, v43, v47 row_shr:2 row_mask:0xf bank_mask:0xf
	v_fmac_f32_dpp v48, v48, v36 row_shr:2 row_mask:0xf bank_mask:0xf
	v_fmac_f32_dpp v49, v49, v37 row_shr:2 row_mask:0xf bank_mask:0xf
	v_fmac_f32_dpp v52, v52, v38 row_shr:2 row_mask:0xf bank_mask:0xf
	v_fmac_f32_dpp v53, v53, v39 row_shr:2 row_mask:0xf bank_mask:0xf
	v_mul_f32_dpp v44, v44, v44 row_shr:2 row_mask:0xf bank_mask:0xf
	v_mul_f32_dpp v45, v45, v45 row_shr:2 row_mask:0xf bank_mask:0xf
	v_mul_f32_dpp v46, v46, v46 row_shr:2 row_mask:0xf bank_mask:0xf
	v_mul_f32_dpp v47, v47, v47 row_shr:2 row_mask:0xf bank_mask:0xf
	v_mul_f32_dpp v36, v36, v36 row_shr:2 row_mask:0xf bank_mask:0xf
	v_mul_f32_dpp v37, v37, v37 row_shr:2 row_mask:0xf bank_mask:0xf
	v_mul_f32_dpp v38, v38, v38 row_shr:2 row_mask:0xf bank_mask:0xf
	v_mul_f32_dpp v39, v39, v39 row_shr:2 row_mask:0xf bank_mask:0xf

;     __device__ __forceinline__ void operator()(AccRef acc, const pg8::Unit& u, int wr, int wc, int fr, int fq) const {
;     ...
;                     GATE_SCAN_STEP(1); GATE_SCAN_STEP(2); GATE_SCAN_STEP(4); GATE_SCAN_STEP(8);
	s_nop 0
	s_nop 1
	v_fmac_f32_dpp v40, v40, v44 row_shr:4 row_mask:0xf bank_mask:0xf
	v_fmac_f32_dpp v41, v41, v45 row_shr:4 row_mask:0xf bank_mask:0xf
	v_fmac_f32_dpp v42, v42, v46 row_shr:4 row_mask:0xf bank_mask:0xf
	v_fmac_f32_dpp v43, v43, v47 row_shr:4 row_mask:0xf bank_mask:0xf
	v_fmac_f32_dpp v48, v48, v36 row_shr:4 row_mask:0xf bank_mask:0xf
	v_fmac_f32_dpp v49, v49, v37 row_shr:4 row_mask:0xf bank_mask:0xf
	v_fmac_f32_dpp v52, v52, v38 row_shr:4 row_mask:0xf bank_mask:0xf
	v_fmac_f32_dpp v53, v53, v39 row_shr:4 row_mask:0xf bank_mask:0xf
	v_mul_f32_dpp v44, v44, v44 row_shr:4 row_mask:0xf bank_mask:0xf
	v_mul_f32_dpp v45, v45, v45 row_shr:4 row_mask:0xf bank_mask:0xf
	v_mul_f32_dpp v46, v46, v46 row_shr:4 row_mask:0xf bank_mask:0xf
	v_mul_f32_dpp v47, v47, v47 row_shr:4 row_mask:0xf bank_mask:0xf
	v_mul_f32_dpp v36, v36, v36 row_shr:4 row_mask:0xf bank_mask:0xf
	v_mul_f32_dpp v37, v37, v37 row_shr:4 row_mask:0xf bank_mask:0xf
	v_mul_f32_dpp v38, v38, v38 row_shr:4 row_mask:0xf bank_mask:0xf
	v_mul_f32_dpp v39, v39, v39 row_shr:4 row_mask:0xf bank_mask:0xf

;     __device__ __forceinline__ void operator()(AccRef acc, const pg8::Unit& u, int wr, int wc, int fr, int fq) const {
;     ...
;                     GATE_SCAN_STEP(1); GATE_SCAN_STEP(2); GATE_SCAN_STEP(4); GATE_SCAN_STEP(8);
	s_nop 0
	s_nop 1
	v_fmac_f32_dpp v40, v40, v44 row_shr:8 row_mask:0xf bank_mask:0xf
	v_fmac_f32_dpp v41, v41, v45 row_shr:8 row_mask:0xf bank_mask:0xf
	v_fmac_f32_dpp v42, v42, v46 row_shr:8 row_mask:0xf bank_mask:0xf
	v_fmac_f32_dpp v43, v43, v47 row_shr:8 row_mask:0xf bank_mask:0xf
	v_fmac_f32_dpp v48, v48, v36 row_shr:8 row_mask:0xf bank_mask:0xf
	v_fmac_f32_dpp v49, v49, v37 row_shr:8 row_mask:0xf bank_mask:0xf
	v_fmac_f32_dpp v52, v52, v38 row_shr:8 row_mask:0xf bank_mask:0xf
	v_fmac_f32_dpp v53, v53, v39 row_shr:8 row_mask:0xf bank_mask:0xf
	v_mul_f32_dpp v44, v44, v44 row_shr:8 row_mask:0xf bank_mask:0xf
	v_mul_f32_dpp v45, v45, v45 row_shr:8 row_mask:0xf bank_mask:0xf
	v_mul_f32_dpp v46, v46, v46 row_shr:8 row_mask:0xf bank_mask:0xf
	v_mul_f32_dpp v47, v47, v47 row_shr:8 row_mask:0xf bank_mask:0xf
	v_mul_f32_dpp v36, v36, v36 row_shr:8 row_mask:0xf bank_mask:0xf
	v_mul_f32_dpp v37, v37, v37 row_shr:8 row_mask:0xf bank_mask:0xf
	v_mul_f32_dpp v38, v38, v38 row_shr:8 row_mask:0xf bank_mask:0xf
	v_mul_f32_dpp v39, v39, v39 row_shr:8 row_mask:0xf bank_mask:0xf

;     __device__ __forceinline__ void operator()(AccRef acc, const pg8::Unit& u, int wr, int wc, int fr, int fq) const {
;     ...
; #pragma unroll
;                     for (int q = 0; q < 4; ++q) {
;                         const float A1 = __int_as_float(__builtin_amdgcn_ds_bpermute(l15, __float_as_int(A[q]))), H1 = __int_as_float(__builtin_amdgcn_ds_bpermute(l15, __float_as_int(B[q])));
;                         B[4 + q] = fmaf(A[4 + q], H1, B[4 + q]); A[4 + q] *= A1; }
; #pragma unroll
;                     for (int sg = 0; sg < 2; ++sg) { const size_t ro = (size_t)(row0 + ai * 128 + (2 * mp + sg) * 16) * RW + ch;
;                         *(f32x4*)(SA + ro) = (f32x4){A[sg * 4], A[sg * 4 + 1], A[sg * 4 + 2], A[sg * 4 + 3]}; *(f32x4*)(SB + ro) = (f32x4){B[sg * 4], B[sg * 4 + 1], B[sg * 4 + 2], B[sg * 4 + 3]}; }
;                     if (fr == 15) { const size_t so = (size_t)(u.pm * 8 + ai * 4 + wr * 2 + mp) * RW + ch;
;                         *(f32x4*)(sumA + so) = (f32x4){A[4], A[5], A[6], A[7]}; *(f32x4*)(sumH + so) = (f32x4){B[4], B[5], B[6], B[7]}; }
	ds_bpermute_b32 v32, v168, v44
	ds_bpermute_b32 v50, v168, v40
	ds_bpermute_b32 v33, v168, v45
	ds_bpermute_b32 v51, v168, v41
	ds_bpermute_b32 v34, v168, v46
	ds_bpermute_b32 v54, v168, v42
	ds_bpermute_b32 v35, v168, v47
	ds_bpermute_b32 v55, v168, v43
	global_store_dwordx4 v[58:59], v[44:47], off
	s_waitcnt lgkmcnt(0)
	v_pk_mul_f32 v[32:33], v[36:37], v[32:33]
	v_pk_fma_f32 v[36:37], v[36:37], v[50:51], v[48:49]
	v_lshl_add_u64 v[44:45], s[8:9], 0, v[56:57]
	global_store_dwordx4 v[44:45], v[40:43], off
	v_pk_mul_f32 v[34:35], v[38:39], v[34:35]
	v_pk_fma_f32 v[38:39], v[38:39], v[54:55], v[52:53]
	v_lshl_add_u64 v[40:41], v[116:117], 0, v[84:85]
	v_lshlrev_b64 v[40:41], 2, v[40:41]
	v_lshl_add_u64 v[42:43], s[6:7], 0, v[40:41]
	v_lshl_add_u64 v[40:41], s[8:9], 0, v[40:41]
	global_store_dwordx4 v[42:43], v[32:35], off
	global_store_dwordx4 v[40:41], v[36:39], off
	s_and_saveexec_b64 s[28:29], s[0:1]
	s_cbranch_execz .LBB0_593
	s_lshl_b32 s56, s46, 3
	s_add_i32 s74, s56, s95
	s_ashr_i32 s75, s74, 31
	s_lshl_b64 s[74:75], s[74:75], 9
	v_lshl_add_u64 v[40:41], s[74:75], 0, v[84:85]
	v_lshlrev_b64 v[40:41], 2, v[40:41]
	v_lshl_add_u64 v[42:43], s[18:19], 0, v[40:41]
	global_store_dwordx4 v[42:43], v[32:35], off
	s_nop 1
	v_lshl_add_u64 v[32:33], s[20:21], 0, v[40:41]
	global_store_dwordx4 v[32:33], v[36:39], off
; __device__ __forceinline__ float bflo(unsigned w) { return __uint_as_float(w << 16); }
; __device__ __forceinline__ float bfhi(unsigned w) { return __uint_as_float(w & 0xffff0000u); }
; __device__ __forceinline__ float sigmoidf_(float x) { return __builtin_amdgcn_rcpf(1.f + __expf(-x)); }
;     __device__ __forceinline__ void operator()(AccRef acc, const pg8::Unit& u, int wr, int wc, int fr, int fq) const {
;     ...
;                 for (int mp = 0; mp < 2; ++mp) {
;                     float A[8], B[8];
; #pragma unroll
;                     for (int sg = 0; sg < 2; ++sg) { const int m = 2 * mp + sg;
;                         const size_t ro = (size_t)(row0 + ai * 128 + m * 16) * RW + ch;
;                         const u32x2 xw = *(const u32x2*)(XC + ro);
;                         const float xc[4] = {bflo(xw.x), bfhi(xw.x), bflo(xw.y), bfhi(xw.y)};
;                         const f32x4 ar = acc[ai][0][m][n], ain = acc[ai][1][m][n];
; #pragma unroll
;                         for (int q = 0; q < 4; ++q) {
;                             const float r = sigmoidf_(ar[q] + vba[q]), ig = sigmoidf_(ain[q] + vbx[q]);
;                             const float la = -r * vsp[q];
;                             const float a = __expf(la);
;                             A[sg * 4 + q] = a; B[sg * 4 + q] = __builtin_amdgcn_sqrtf((1.f - a) * (1.f + a)) * (ig * xc[q]);
;                         }
;                     }
;     ...
;                     GATE_SCAN_STEP(1); GATE_SCAN_STEP(2); GATE_SCAN_STEP(4); GATE_SCAN_STEP(8);
.LBB0_593:
	s_or_b64 exec, exec, s[28:29]
	v_lshl_add_u64 v[32:33], s[10:11], 0, v[108:109]
	v_lshl_add_u64 v[32:33], v[32:33], 0, v[86:87]
	s_nop 0
	v_add_f32_e32 v28, v28, v242
	v_mul_f32_e32 v28, 0xbfb8aa3b, v28
	v_exp_f32_e32 v28, v28
	v_add_f32_e32 v29, v29, v243
	v_mul_f32_e32 v29, 0xbfb8aa3b, v29
	v_exp_f32_e32 v29, v29
	v_add_f32_e32 v28, 1.0, v28
	v_rcp_f32_e32 v28, v28
	v_add_f32_e32 v24, v24, v246
	v_mul_f32_e32 v24, 0xbfb8aa3b, v24
	v_add_f32_e32 v29, 1.0, v29
	v_mul_f32_e32 v28, v250, v28
	v_mul_f32_e32 v28, 0xbfb8aa3b, v28
	v_add_f32_e32 v30, v30, v244
	v_exp_f32_e32 v24, v24
	v_exp_f32_e32 v28, v28
	v_rcp_f32_e32 v29, v29
	v_mul_f32_e32 v30, 0xbfb8aa3b, v30
	v_exp_f32_e32 v30, v30
	v_add_f32_e32 v24, 1.0, v24
	v_sub_f32_e32 v36, 1.0, v28
	v_add_f32_e32 v37, 1.0, v28
	v_add_f32_e32 v25, v25, v247
	v_mul_f32_e32 v29, v251, v29
	v_rcp_f32_e32 v24, v24
	v_mul_f32_e32 v36, v36, v37
	v_mul_f32_e32 v25, 0xbfb8aa3b, v25
	v_mul_f32_e32 v29, 0xbfb8aa3b, v29
	v_add_f32_e32 v30, 1.0, v30
	v_add_f32_e32 v31, v31, v245
	v_sqrt_f32_e32 v36, v36
	v_exp_f32_e32 v25, v25
	v_exp_f32_e32 v29, v29
	v_rcp_f32_e32 v30, v30
	v_mul_f32_e32 v31, 0xbfb8aa3b, v31
	v_exp_f32_e32 v31, v31
	v_add_f32_e32 v25, 1.0, v25
	v_add_f32_e32 v26, v26, v248
	v_mul_f32_e32 v30, v252, v30
	v_rcp_f32_e32 v25, v25
	v_mul_f32_e32 v26, 0xbfb8aa3b, v26
	v_mul_f32_e32 v30, 0xbfb8aa3b, v30
	v_add_f32_e32 v31, 1.0, v31
	v_exp_f32_e32 v26, v26
	v_exp_f32_e32 v30, v30
	v_rcp_f32_e32 v31, v31
	v_add_f32_e32 v27, v27, v249
	v_add_f32_e32 v26, 1.0, v26
	v_rcp_f32_e32 v26, v26
	v_mul_f32_e32 v31, v253, v31
	v_mul_f32_e32 v27, 0xbfb8aa3b, v27
	v_mul_f32_e32 v31, 0xbfb8aa3b, v31
	v_exp_f32_e32 v27, v27
	v_exp_f32_e32 v31, v31
	v_add_f32_e32 v20, v20, v242
	v_mul_f32_e32 v20, 0xbfb8aa3b, v20
	v_add_f32_e32 v27, 1.0, v27
	v_rcp_f32_e32 v27, v27
	v_exp_f32_e32 v20, v20
	v_add_f32_e32 v16, v16, v246
	v_mul_f32_e32 v16, 0xbfb8aa3b, v16
	v_exp_f32_e32 v16, v16
	v_add_f32_e32 v20, 1.0, v20
	v_rcp_f32_e32 v20, v20
	v_add_f32_e32 v17, v17, v247
	v_add_f32_e32 v16, 1.0, v16
	v_rcp_f32_e32 v16, v16
	v_mul_f32_e32 v20, v250, v20
	v_mul_f32_e32 v20, 0xbfb8aa3b, v20
	v_exp_f32_e32 v20, v20
	v_mul_f32_e32 v17, 0xbfb8aa3b, v17
	v_exp_f32_e32 v17, v17
	v_lshl_add_u64 v[40:41], v[112:113], 0, v[84:85]
	v_lshlrev_b64 v[40:41], 2, v[40:41]
	v_lshl_add_u64 v[42:43], s[6:7], 0, v[40:41]
	v_add_f32_e32 v17, 1.0, v17
	v_rcp_f32_e32 v17, v17
	s_waitcnt lgkmcnt(0)
	v_lshlrev_b32_e32 v34, 16, v228
	v_mul_f32_e32 v24, v24, v34
	v_mul_f32_e32 v24, v36, v24
	v_sub_f32_e32 v34, 1.0, v29
	v_add_f32_e32 v36, 1.0, v29
	v_mul_f32_e32 v34, v34, v36
	v_sqrt_f32_e32 v34, v34
	v_and_b32_e32 v32, 0xffff0000, v228
	v_mul_f32_e32 v25, v25, v32
	v_sub_f32_e32 v32, 1.0, v30
	v_mul_f32_e32 v25, v34, v25
	v_add_f32_e32 v34, 1.0, v30
	v_mul_f32_e32 v32, v32, v34
	v_sqrt_f32_e32 v32, v32
	v_lshlrev_b32_e32 v35, 16, v229
	v_mul_f32_e32 v26, v26, v35
	v_add_f32_e32 v34, 1.0, v31
	v_mul_f32_e32 v26, v32, v26
	v_sub_f32_e32 v32, 1.0, v31
	v_mul_f32_e32 v32, v32, v34
	v_sqrt_f32_e32 v32, v32
	v_and_b32_e32 v33, 0xffff0000, v229
	v_mul_f32_e32 v27, v27, v33
	v_mul_f32_e32 v27, v32, v27
	v_lshl_add_u64 v[32:33], s[10:11], 0, v[110:111]
	v_lshl_add_u64 v[32:33], v[32:33], 0, v[86:87]
	s_nop 0
	s_waitcnt lgkmcnt(0)
	v_lshlrev_b32_e32 v35, 16, v230
	v_and_b32_e32 v36, 0xffff0000, v230
	v_lshlrev_b32_e32 v37, 16, v231
	v_and_b32_e32 v34, 0xffff0000, v231
	v_sub_f32_e32 v32, 1.0, v20
	v_add_f32_e32 v33, 1.0, v20
	v_mul_f32_e32 v32, v32, v33
	v_sqrt_f32_e32 v32, v32
	v_mul_f32_e32 v16, v16, v35
	v_mul_f32_e32 v17, v17, v36
	v_mul_f32_e32 v32, v32, v16
	v_add_f32_e32 v16, v21, v243
	v_mul_f32_e32 v16, 0xbfb8aa3b, v16
	v_exp_f32_e32 v16, v16
	s_nop 0
	v_add_f32_e32 v16, 1.0, v16
	v_rcp_f32_e32 v16, v16
	s_nop 0
	v_mul_f32_e32 v16, v251, v16
	v_mul_f32_e32 v16, 0xbfb8aa3b, v16
	v_exp_f32_e32 v21, v16
	s_nop 0
	v_sub_f32_e32 v16, 1.0, v21
	v_add_f32_e32 v33, 1.0, v21
	v_mul_f32_e32 v16, v16, v33
	v_sqrt_f32_e32 v16, v16
	s_nop 0
	v_mul_f32_e32 v33, v16, v17
	v_add_f32_e32 v16, v22, v244
	v_mul_f32_e32 v16, 0xbfb8aa3b, v16
	v_exp_f32_e32 v16, v16
	v_add_f32_e32 v17, v18, v248
	v_mul_f32_e32 v17, 0xbfb8aa3b, v17
	v_exp_f32_e32 v17, v17
	v_add_f32_e32 v16, 1.0, v16
	v_rcp_f32_e32 v16, v16
	v_add_f32_e32 v17, 1.0, v17
	v_rcp_f32_e32 v17, v17
	v_mul_f32_e32 v16, v252, v16
	v_mul_f32_e32 v16, 0xbfb8aa3b, v16
	v_exp_f32_e32 v22, v16
	v_mul_f32_e32 v17, v17, v37
	v_sub_f32_e32 v16, 1.0, v22
	v_add_f32_e32 v18, 1.0, v22
	v_mul_f32_e32 v16, v16, v18
	v_sqrt_f32_e32 v16, v16
	s_nop 0
	v_mul_f32_e32 v36, v16, v17
	v_add_f32_e32 v16, v23, v245
	v_mul_f32_e32 v16, 0xbfb8aa3b, v16
	v_exp_f32_e32 v16, v16
	v_add_f32_e32 v17, v19, v249
	v_mul_f32_e32 v17, 0xbfb8aa3b, v17
	v_exp_f32_e32 v17, v17
	v_add_f32_e32 v16, 1.0, v16
	v_rcp_f32_e32 v16, v16
	v_add_f32_e32 v17, 1.0, v17
	v_rcp_f32_e32 v17, v17
	v_mul_f32_e32 v16, v253, v16
	v_mul_f32_e32 v16, 0xbfb8aa3b, v16
	v_exp_f32_e32 v23, v16
	v_mul_f32_e32 v17, v17, v34
	v_sub_f32_e32 v16, 1.0, v23
	v_add_f32_e32 v18, 1.0, v23
	v_mul_f32_e32 v16, v16, v18
	v_sqrt_f32_e32 v16, v16
	s_nop 0
	v_mul_f32_e32 v37, v16, v17
	s_nop 1
	v_fmac_f32_dpp v24, v24, v28 row_shr:1 row_mask:0xf bank_mask:0xf
	v_fmac_f32_dpp v25, v25, v29 row_shr:1 row_mask:0xf bank_mask:0xf
	v_fmac_f32_dpp v26, v26, v30 row_shr:1 row_mask:0xf bank_mask:0xf
	v_fmac_f32_dpp v27, v27, v31 row_shr:1 row_mask:0xf bank_mask:0xf
	v_fmac_f32_dpp v32, v32, v20 row_shr:1 row_mask:0xf bank_mask:0xf
	v_fmac_f32_dpp v33, v33, v21 row_shr:1 row_mask:0xf bank_mask:0xf
	v_fmac_f32_dpp v36, v36, v22 row_shr:1 row_mask:0xf bank_mask:0xf
	v_fmac_f32_dpp v37, v37, v23 row_shr:1 row_mask:0xf bank_mask:0xf
	v_mul_f32_dpp v28, v28, v28 row_shr:1 row_mask:0xf bank_mask:0xf
	v_mul_f32_dpp v29, v29, v29 row_shr:1 row_mask:0xf bank_mask:0xf
	v_mul_f32_dpp v30, v30, v30 row_shr:1 row_mask:0xf bank_mask:0xf
	v_mul_f32_dpp v31, v31, v31 row_shr:1 row_mask:0xf bank_mask:0xf
	v_mul_f32_dpp v20, v20, v20 row_shr:1 row_mask:0xf bank_mask:0xf
	v_mul_f32_dpp v21, v21, v21 row_shr:1 row_mask:0xf bank_mask:0xf
	v_mul_f32_dpp v22, v22, v22 row_shr:1 row_mask:0xf bank_mask:0xf
	v_mul_f32_dpp v23, v23, v23 row_shr:1 row_mask:0xf bank_mask:0xf

;     __device__ __forceinline__ void operator()(AccRef acc, const pg8::Unit& u, int wr, int wc, int fr, int fq) const {
;     ...
;                     GATE_SCAN_STEP(1); GATE_SCAN_STEP(2); GATE_SCAN_STEP(4); GATE_SCAN_STEP(8);
	s_nop 0
	s_nop 1
	v_fmac_f32_dpp v24, v24, v28 row_shr:2 row_mask:0xf bank_mask:0xf
	v_fmac_f32_dpp v25, v25, v29 row_shr:2 row_mask:0xf bank_mask:0xf
	v_fmac_f32_dpp v26, v26, v30 row_shr:2 row_mask:0xf bank_mask:0xf
	v_fmac_f32_dpp v27, v27, v31 row_shr:2 row_mask:0xf bank_mask:0xf
	v_fmac_f32_dpp v32, v32, v20 row_shr:2 row_mask:0xf bank_mask:0xf
	v_fmac_f32_dpp v33, v33, v21 row_shr:2 row_mask:0xf bank_mask:0xf
	v_fmac_f32_dpp v36, v36, v22 row_shr:2 row_mask:0xf bank_mask:0xf
	v_fmac_f32_dpp v37, v37, v23 row_shr:2 row_mask:0xf bank_mask:0xf
	v_mul_f32_dpp v28, v28, v28 row_shr:2 row_mask:0xf bank_mask:0xf
	v_mul_f32_dpp v29, v29, v29 row_shr:2 row_mask:0xf bank_mask:0xf
	v_mul_f32_dpp v30, v30, v30 row_shr:2 row_mask:0xf bank_mask:0xf
	v_mul_f32_dpp v31, v31, v31 row_shr:2 row_mask:0xf bank_mask:0xf
	v_mul_f32_dpp v20, v20, v20 row_shr:2 row_mask:0xf bank_mask:0xf
	v_mul_f32_dpp v21, v21, v21 row_shr:2 row_mask:0xf bank_mask:0xf
	v_mul_f32_dpp v22, v22, v22 row_shr:2 row_mask:0xf bank_mask:0xf
	v_mul_f32_dpp v23, v23, v23 row_shr:2 row_mask:0xf bank_mask:0xf

;     __device__ __forceinline__ void operator()(AccRef acc, const pg8::Unit& u, int wr, int wc, int fr, int fq) const {
;     ...
;                     GATE_SCAN_STEP(1); GATE_SCAN_STEP(2); GATE_SCAN_STEP(4); GATE_SCAN_STEP(8);
	s_nop 0
	s_nop 1
	v_fmac_f32_dpp v24, v24, v28 row_shr:4 row_mask:0xf bank_mask:0xf
	v_fmac_f32_dpp v25, v25, v29 row_shr:4 row_mask:0xf bank_mask:0xf
	v_fmac_f32_dpp v26, v26, v30 row_shr:4 row_mask:0xf bank_mask:0xf
	v_fmac_f32_dpp v27, v27, v31 row_shr:4 row_mask:0xf bank_mask:0xf
	v_fmac_f32_dpp v32, v32, v20 row_shr:4 row_mask:0xf bank_mask:0xf
	v_fmac_f32_dpp v33, v33, v21 row_shr:4 row_mask:0xf bank_mask:0xf
	v_fmac_f32_dpp v36, v36, v22 row_shr:4 row_mask:0xf bank_mask:0xf
	v_fmac_f32_dpp v37, v37, v23 row_shr:4 row_mask:0xf bank_mask:0xf
	v_mul_f32_dpp v28, v28, v28 row_shr:4 row_mask:0xf bank_mask:0xf
	v_mul_f32_dpp v29, v29, v29 row_shr:4 row_mask:0xf bank_mask:0xf
	v_mul_f32_dpp v30, v30, v30 row_shr:4 row_mask:0xf bank_mask:0xf
	v_mul_f32_dpp v31, v31, v31 row_shr:4 row_mask:0xf bank_mask:0xf
	v_mul_f32_dpp v20, v20, v20 row_shr:4 row_mask:0xf bank_mask:0xf
	v_mul_f32_dpp v21, v21, v21 row_shr:4 row_mask:0xf bank_mask:0xf
	v_mul_f32_dpp v22, v22, v22 row_shr:4 row_mask:0xf bank_mask:0xf
	v_mul_f32_dpp v23, v23, v23 row_shr:4 row_mask:0xf bank_mask:0xf

;     __device__ __forceinline__ void operator()(AccRef acc, const pg8::Unit& u, int wr, int wc, int fr, int fq) const {
;     ...
;                     GATE_SCAN_STEP(1); GATE_SCAN_STEP(2); GATE_SCAN_STEP(4); GATE_SCAN_STEP(8);
	s_nop 0
	s_nop 1
	v_fmac_f32_dpp v24, v24, v28 row_shr:8 row_mask:0xf bank_mask:0xf
	v_fmac_f32_dpp v25, v25, v29 row_shr:8 row_mask:0xf bank_mask:0xf
	v_fmac_f32_dpp v26, v26, v30 row_shr:8 row_mask:0xf bank_mask:0xf
	v_fmac_f32_dpp v27, v27, v31 row_shr:8 row_mask:0xf bank_mask:0xf
	v_fmac_f32_dpp v32, v32, v20 row_shr:8 row_mask:0xf bank_mask:0xf
	v_fmac_f32_dpp v33, v33, v21 row_shr:8 row_mask:0xf bank_mask:0xf
	v_fmac_f32_dpp v36, v36, v22 row_shr:8 row_mask:0xf bank_mask:0xf
	v_fmac_f32_dpp v37, v37, v23 row_shr:8 row_mask:0xf bank_mask:0xf
	v_mul_f32_dpp v28, v28, v28 row_shr:8 row_mask:0xf bank_mask:0xf
	v_mul_f32_dpp v29, v29, v29 row_shr:8 row_mask:0xf bank_mask:0xf
	v_mul_f32_dpp v30, v30, v30 row_shr:8 row_mask:0xf bank_mask:0xf
	v_mul_f32_dpp v31, v31, v31 row_shr:8 row_mask:0xf bank_mask:0xf
	v_mul_f32_dpp v20, v20, v20 row_shr:8 row_mask:0xf bank_mask:0xf
	v_mul_f32_dpp v21, v21, v21 row_shr:8 row_mask:0xf bank_mask:0xf
	v_mul_f32_dpp v22, v22, v22 row_shr:8 row_mask:0xf bank_mask:0xf
	v_mul_f32_dpp v23, v23, v23 row_shr:8 row_mask:0xf bank_mask:0xf

;     __device__ __forceinline__ void operator()(AccRef acc, const pg8::Unit& u, int wr, int wc, int fr, int fq) const {
;     ...
; #pragma unroll
;                     for (int q = 0; q < 4; ++q) {
;                         const float A1 = __int_as_float(__builtin_amdgcn_ds_bpermute(l15, __float_as_int(A[q]))), H1 = __int_as_float(__builtin_amdgcn_ds_bpermute(l15, __float_as_int(B[q])));
;                         B[4 + q] = fmaf(A[4 + q], H1, B[4 + q]); A[4 + q] *= A1; }
; #pragma unroll
;                     for (int sg = 0; sg < 2; ++sg) { const size_t ro = (size_t)(row0 + ai * 128 + (2 * mp + sg) * 16) * RW + ch;
;                         *(f32x4*)(SA + ro) = (f32x4){A[sg * 4], A[sg * 4 + 1], A[sg * 4 + 2], A[sg * 4 + 3]}; *(f32x4*)(SB + ro) = (f32x4){B[sg * 4], B[sg * 4 + 1], B[sg * 4 + 2], B[sg * 4 + 3]}; }
;                     if (fr == 15) { const size_t so = (size_t)(u.pm * 8 + ai * 4 + wr * 2 + mp) * RW + ch;
;                         *(f32x4*)(sumA + so) = (f32x4){A[4], A[5], A[6], A[7]}; *(f32x4*)(sumH + so) = (f32x4){B[4], B[5], B[6], B[7]}; }
	ds_bpermute_b32 v16, v168, v28
	ds_bpermute_b32 v34, v168, v24
	ds_bpermute_b32 v17, v168, v29
	ds_bpermute_b32 v35, v168, v25
	ds_bpermute_b32 v18, v168, v30
	ds_bpermute_b32 v38, v168, v26
	ds_bpermute_b32 v19, v168, v31
	ds_bpermute_b32 v39, v168, v27
	global_store_dwordx4 v[42:43], v[28:31], off
	s_waitcnt lgkmcnt(0)
	v_pk_mul_f32 v[16:17], v[20:21], v[16:17]
	v_pk_fma_f32 v[20:21], v[20:21], v[34:35], v[32:33]
	v_lshl_add_u64 v[28:29], s[8:9], 0, v[40:41]
	global_store_dwordx4 v[28:29], v[24:27], off
	v_pk_mul_f32 v[18:19], v[22:23], v[18:19]
	v_pk_fma_f32 v[22:23], v[22:23], v[38:39], v[36:37]
	v_lshl_add_u64 v[24:25], v[100:101], 0, v[84:85]
	v_lshlrev_b64 v[24:25], 2, v[24:25]
	v_lshl_add_u64 v[26:27], s[6:7], 0, v[24:25]
	v_lshl_add_u64 v[24:25], s[8:9], 0, v[24:25]
	global_store_dwordx4 v[26:27], v[16:19], off
	global_store_dwordx4 v[24:25], v[20:23], off
	s_and_saveexec_b64 s[28:29], s[0:1]
	s_cbranch_execz .LBB0_595
	s_lshl_b32 s56, s46, 3
	s_add_i32 s74, s56, s96
	s_ashr_i32 s75, s74, 31
	s_lshl_b64 s[74:75], s[74:75], 9
	v_lshl_add_u64 v[24:25], s[74:75], 0, v[84:85]
	v_lshlrev_b64 v[24:25], 2, v[24:25]
	v_lshl_add_u64 v[26:27], s[18:19], 0, v[24:25]
	global_store_dwordx4 v[26:27], v[16:19], off
	s_nop 1
	v_lshl_add_u64 v[16:17], s[20:21], 0, v[24:25]
	global_store_dwordx4 v[16:17], v[20:23], off
; __device__ __forceinline__ float bflo(unsigned w) { return __uint_as_float(w << 16); }
; __device__ __forceinline__ float bfhi(unsigned w) { return __uint_as_float(w & 0xffff0000u); }
; __device__ __forceinline__ float sigmoidf_(float x) { return __builtin_amdgcn_rcpf(1.f + __expf(-x)); }
;     __device__ __forceinline__ void operator()(AccRef acc, const pg8::Unit& u, int wr, int wc, int fr, int fq) const {
;     ...
;                     for (int sg = 0; sg < 2; ++sg) { const int m = 2 * mp + sg;
;                         const size_t ro = (size_t)(row0 + ai * 128 + m * 16) * RW + ch;
;                         const u32x2 xw = *(const u32x2*)(XC + ro);
;                         const float xc[4] = {bflo(xw.x), bfhi(xw.x), bflo(xw.y), bfhi(xw.y)};
;                         const f32x4 ar = acc[ai][0][m][n], ain = acc[ai][1][m][n];
; #pragma unroll
;                         for (int q = 0; q < 4; ++q) {
;                             const float r = sigmoidf_(ar[q] + vba[q]), ig = sigmoidf_(ain[q] + vbx[q]);
;                             const float la = -r * vsp[q];
;                             const float a = __expf(la);
;                             A[sg * 4 + q] = a; B[sg * 4 + q] = __builtin_amdgcn_sqrtf((1.f - a) * (1.f + a)) * (ig * xc[q]);
;                         }
;                     }
;     ...
;                     GATE_SCAN_STEP(1); GATE_SCAN_STEP(2); GATE_SCAN_STEP(4); GATE_SCAN_STEP(8);
.LBB0_595:
	s_or_b64 exec, exec, s[28:29]
	v_lshl_add_u64 v[16:17], s[10:11], 0, v[80:81]
	v_lshl_add_u64 v[16:17], v[16:17], 0, v[86:87]
	s_nop 0
	v_add_f32_e32 v20, v8, v246
	v_add_f32_e32 v21, v9, v247
	v_lshl_add_u64 v[8:9], s[10:11], 0, v[76:77]
	v_lshl_add_u64 v[8:9], v[8:9], 0, v[86:87]
	s_nop 0
	v_add_f32_e32 v12, v12, v242
	v_add_f32_e32 v13, v13, v243
	v_add_f32_e32 v8, v14, v244
	v_add_f32_e32 v9, v10, v248
	v_add_f32_e32 v10, v15, v245
	v_mul_f32_e32 v12, 0xbfb8aa3b, v12
	v_mul_f32_e32 v13, 0xbfb8aa3b, v13
	v_mul_f32_e32 v8, 0xbfb8aa3b, v8
	v_mul_f32_e32 v9, 0xbfb8aa3b, v9
	v_mul_f32_e32 v10, 0xbfb8aa3b, v10
	v_exp_f32_e32 v12, v12
	v_exp_f32_e32 v13, v13
	v_exp_f32_e32 v8, v8
	v_exp_f32_e32 v9, v9
	v_exp_f32_e32 v10, v10
	v_add_f32_e32 v11, v11, v249
	v_mul_f32_e32 v11, 0xbfb8aa3b, v11
	v_exp_f32_e32 v11, v11
	v_add_f32_e32 v12, 1.0, v12
	v_add_f32_e32 v13, 1.0, v13
	v_add_f32_e32 v4, v4, v242
	v_add_f32_e32 v8, 1.0, v8
	v_add_f32_e32 v9, 1.0, v9
	v_add_f32_e32 v10, 1.0, v10
	v_rcp_f32_e32 v12, v12
	v_rcp_f32_e32 v13, v13
	v_mul_f32_e32 v4, 0xbfb8aa3b, v4
	v_mul_f32_e32 v14, 0xbfb8aa3b, v20
	v_rcp_f32_e32 v8, v8
	v_rcp_f32_e32 v20, v9
	v_rcp_f32_e32 v9, v10
	v_exp_f32_e32 v4, v4
	v_add_f32_e32 v11, 1.0, v11
	v_mul_f32_e32 v15, 0xbfb8aa3b, v21
	v_rcp_f32_e32 v21, v11
	v_mul_f32_e32 v10, v250, v12
	v_mul_f32_e32 v11, v251, v13
	v_mul_f32_e32 v8, v252, v8
	v_mul_f32_e32 v9, v253, v9
	v_mul_f32_e32 v10, 0xbfb8aa3b, v10
	v_mul_f32_e32 v11, 0xbfb8aa3b, v11
	v_add_f32_e32 v4, 1.0, v4
	v_add_f32_e32 v5, v5, v243
	v_exp_f32_e32 v15, v15
	v_mul_f32_e32 v12, 0xbfb8aa3b, v8
	v_mul_f32_e32 v13, 0xbfb8aa3b, v9
	v_exp_f32_e32 v8, v10
	v_exp_f32_e32 v9, v11
	v_rcp_f32_e32 v4, v4
	v_mul_f32_e32 v5, 0xbfb8aa3b, v5
	v_exp_f32_e32 v5, v5
	v_exp_f32_e32 v10, v12
	v_exp_f32_e32 v14, v14
	v_add_f32_e32 v15, 1.0, v15
	v_exp_f32_e32 v11, v13
	v_sub_f32_e32 v12, 1.0, v8
	v_add_f32_e32 v13, 1.0, v8
	v_sub_f32_e32 v22, 1.0, v9
	v_add_f32_e32 v23, 1.0, v9
	v_add_f32_e32 v0, v0, v246
	v_mul_f32_e32 v4, v250, v4
	v_rcp_f32_e32 v15, v15
	v_mul_f32_e32 v12, v12, v13
	v_mul_f32_e32 v13, v22, v23
	v_mul_f32_e32 v0, 0xbfb8aa3b, v0
	v_mul_f32_e32 v4, 0xbfb8aa3b, v4
	v_add_f32_e32 v5, 1.0, v5
	v_sqrt_f32_e32 v13, v13
	v_exp_f32_e32 v0, v0
	v_exp_f32_e32 v4, v4
	v_rcp_f32_e32 v5, v5
	v_sub_f32_e32 v24, 1.0, v10
	v_add_f32_e32 v25, 1.0, v10
	v_add_f32_e32 v14, 1.0, v14
	v_mul_f32_e32 v22, v24, v25
	s_waitcnt lgkmcnt(0)
	v_lshlrev_b32_e32 v24, 16, v232
	v_and_b32_e32 v16, 0xffff0000, v232
	v_rcp_f32_e32 v14, v14
	v_lshlrev_b32_e32 v25, 16, v233
	v_and_b32_e32 v17, 0xffff0000, v233
	v_mul_f32_e32 v15, v15, v16
	v_sqrt_f32_e32 v12, v12
	v_sqrt_f32_e32 v22, v22
	v_mul_f32_e32 v16, v20, v25
	v_mul_f32_e32 v13, v13, v15
	v_mul_f32_e32 v15, v21, v17
	v_add_f32_e32 v0, 1.0, v0
	v_sub_f32_e32 v20, 1.0, v4
	v_add_f32_e32 v21, 1.0, v4
	v_add_f32_e32 v1, v1, v247
	v_mul_f32_e32 v5, v251, v5
	v_rcp_f32_e32 v0, v0
	v_mul_f32_e32 v20, v20, v21
	v_mul_f32_e32 v1, 0xbfb8aa3b, v1
	v_mul_f32_e32 v5, 0xbfb8aa3b, v5
	v_add_f32_e32 v6, v6, v244
	v_sqrt_f32_e32 v20, v20
	v_exp_f32_e32 v1, v1
	v_exp_f32_e32 v5, v5
	v_mul_f32_e32 v6, 0xbfb8aa3b, v6
	v_mul_f32_e32 v14, v14, v24
	v_exp_f32_e32 v6, v6
	v_mul_f32_e32 v12, v12, v14
	v_mul_f32_e32 v14, v22, v16
	v_lshlrev_b32_e32 v16, 16, v234
	v_mul_f32_e32 v0, v0, v16
	v_mul_f32_e32 v16, v20, v0
	v_add_f32_e32 v0, 1.0, v1
	v_sub_f32_e32 v1, 1.0, v5
	v_add_f32_e32 v20, 1.0, v5
	v_rcp_f32_e32 v0, v0
	v_mul_f32_e32 v1, v1, v20
	v_add_f32_e32 v6, 1.0, v6
	v_sqrt_f32_e32 v1, v1
	v_rcp_f32_e32 v6, v6
	v_and_b32_e32 v17, 0xffff0000, v234
	v_mul_f32_e32 v0, v0, v17
	v_mul_f32_e32 v17, v1, v0
	v_mul_f32_e32 v1, v252, v6
	v_mul_f32_e32 v1, 0xbfb8aa3b, v1
	v_exp_f32_e32 v6, v1
	v_add_f32_e32 v1, v7, v245
	v_mul_f32_e32 v1, 0xbfb8aa3b, v1
	v_exp_f32_e32 v1, v1
	v_add_f32_e32 v2, v2, v248
	v_mul_f32_e32 v2, 0xbfb8aa3b, v2
	v_exp_f32_e32 v2, v2
	v_add_f32_e32 v1, 1.0, v1
	v_rcp_f32_e32 v1, v1
	v_add_f32_e32 v3, v3, v249
	v_add_f32_e32 v0, 1.0, v2
	v_sub_f32_e32 v2, 1.0, v6
	v_mul_f32_e32 v1, v253, v1
	v_add_f32_e32 v7, 1.0, v6
	v_mul_f32_e32 v3, 0xbfb8aa3b, v3
	v_mul_f32_e32 v1, 0xbfb8aa3b, v1
	v_mul_f32_e32 v2, v2, v7
	v_exp_f32_e32 v3, v3
	v_exp_f32_e32 v7, v1
	v_sub_f32_e32 v26, 1.0, v11
	v_add_f32_e32 v27, 1.0, v11
	v_rcp_f32_e32 v0, v0
	v_sqrt_f32_e32 v1, v2
	v_add_f32_e32 v2, 1.0, v3
	v_sub_f32_e32 v3, 1.0, v7
	v_add_f32_e32 v20, 1.0, v7
	v_mul_f32_e32 v23, v26, v27
	v_rcp_f32_e32 v2, v2
	v_mul_f32_e32 v3, v3, v20
	v_sqrt_f32_e32 v23, v23
	v_sqrt_f32_e32 v3, v3
	v_lshlrev_b32_e32 v18, 16, v235
	v_and_b32_e32 v19, 0xffff0000, v235
	v_mul_f32_e32 v0, v0, v18
	v_mul_f32_e32 v18, v1, v0
	v_mul_f32_e32 v0, v2, v19
	v_mul_f32_e32 v15, v23, v15
	v_mul_f32_e32 v19, v3, v0
	s_nop 1
	v_fmac_f32_dpp v12, v12, v8 row_shr:1 row_mask:0xf bank_mask:0xf
	v_fmac_f32_dpp v13, v13, v9 row_shr:1 row_mask:0xf bank_mask:0xf
	v_fmac_f32_dpp v14, v14, v10 row_shr:1 row_mask:0xf bank_mask:0xf
	v_fmac_f32_dpp v15, v15, v11 row_shr:1 row_mask:0xf bank_mask:0xf
	v_fmac_f32_dpp v16, v16, v4 row_shr:1 row_mask:0xf bank_mask:0xf
	v_fmac_f32_dpp v17, v17, v5 row_shr:1 row_mask:0xf bank_mask:0xf
	v_fmac_f32_dpp v18, v18, v6 row_shr:1 row_mask:0xf bank_mask:0xf
	v_fmac_f32_dpp v19, v19, v7 row_shr:1 row_mask:0xf bank_mask:0xf
	v_mul_f32_dpp v8, v8, v8 row_shr:1 row_mask:0xf bank_mask:0xf
	v_mul_f32_dpp v9, v9, v9 row_shr:1 row_mask:0xf bank_mask:0xf
	v_mul_f32_dpp v10, v10, v10 row_shr:1 row_mask:0xf bank_mask:0xf
	v_mul_f32_dpp v11, v11, v11 row_shr:1 row_mask:0xf bank_mask:0xf
	v_mul_f32_dpp v4, v4, v4 row_shr:1 row_mask:0xf bank_mask:0xf
	v_mul_f32_dpp v5, v5, v5 row_shr:1 row_mask:0xf bank_mask:0xf
	v_mul_f32_dpp v6, v6, v6 row_shr:1 row_mask:0xf bank_mask:0xf
	v_mul_f32_dpp v7, v7, v7 row_shr:1 row_mask:0xf bank_mask:0xf

;     __device__ __forceinline__ void operator()(AccRef acc, const pg8::Unit& u, int wr, int wc, int fr, int fq) const {
;     ...
;                     GATE_SCAN_STEP(1); GATE_SCAN_STEP(2); GATE_SCAN_STEP(4); GATE_SCAN_STEP(8);
	v_lshl_add_u64 v[24:25], v[78:79], 0, v[84:85]
	s_nop 1
	v_fmac_f32_dpp v12, v12, v8 row_shr:2 row_mask:0xf bank_mask:0xf
	v_fmac_f32_dpp v13, v13, v9 row_shr:2 row_mask:0xf bank_mask:0xf
	v_fmac_f32_dpp v14, v14, v10 row_shr:2 row_mask:0xf bank_mask:0xf
	v_fmac_f32_dpp v15, v15, v11 row_shr:2 row_mask:0xf bank_mask:0xf
	v_fmac_f32_dpp v16, v16, v4 row_shr:2 row_mask:0xf bank_mask:0xf
	v_fmac_f32_dpp v17, v17, v5 row_shr:2 row_mask:0xf bank_mask:0xf
	v_fmac_f32_dpp v18, v18, v6 row_shr:2 row_mask:0xf bank_mask:0xf
	v_fmac_f32_dpp v19, v19, v7 row_shr:2 row_mask:0xf bank_mask:0xf
	v_mul_f32_dpp v8, v8, v8 row_shr:2 row_mask:0xf bank_mask:0xf
	v_mul_f32_dpp v9, v9, v9 row_shr:2 row_mask:0xf bank_mask:0xf
	v_mul_f32_dpp v10, v10, v10 row_shr:2 row_mask:0xf bank_mask:0xf
	v_mul_f32_dpp v11, v11, v11 row_shr:2 row_mask:0xf bank_mask:0xf
	v_mul_f32_dpp v4, v4, v4 row_shr:2 row_mask:0xf bank_mask:0xf
	v_mul_f32_dpp v5, v5, v5 row_shr:2 row_mask:0xf bank_mask:0xf
	v_mul_f32_dpp v6, v6, v6 row_shr:2 row_mask:0xf bank_mask:0xf
	v_mul_f32_dpp v7, v7, v7 row_shr:2 row_mask:0xf bank_mask:0xf

;     __device__ __forceinline__ void operator()(AccRef acc, const pg8::Unit& u, int wr, int wc, int fr, int fq) const {
;     ...
;                     GATE_SCAN_STEP(1); GATE_SCAN_STEP(2); GATE_SCAN_STEP(4); GATE_SCAN_STEP(8);
	v_lshlrev_b64 v[24:25], 2, v[24:25]
	s_nop 1
	v_fmac_f32_dpp v12, v12, v8 row_shr:4 row_mask:0xf bank_mask:0xf
	v_fmac_f32_dpp v13, v13, v9 row_shr:4 row_mask:0xf bank_mask:0xf
	v_fmac_f32_dpp v14, v14, v10 row_shr:4 row_mask:0xf bank_mask:0xf
	v_fmac_f32_dpp v15, v15, v11 row_shr:4 row_mask:0xf bank_mask:0xf
	v_fmac_f32_dpp v16, v16, v4 row_shr:4 row_mask:0xf bank_mask:0xf
	v_fmac_f32_dpp v17, v17, v5 row_shr:4 row_mask:0xf bank_mask:0xf
	v_fmac_f32_dpp v18, v18, v6 row_shr:4 row_mask:0xf bank_mask:0xf
	v_fmac_f32_dpp v19, v19, v7 row_shr:4 row_mask:0xf bank_mask:0xf
	v_mul_f32_dpp v8, v8, v8 row_shr:4 row_mask:0xf bank_mask:0xf
	v_mul_f32_dpp v9, v9, v9 row_shr:4 row_mask:0xf bank_mask:0xf
	v_mul_f32_dpp v10, v10, v10 row_shr:4 row_mask:0xf bank_mask:0xf
	v_mul_f32_dpp v11, v11, v11 row_shr:4 row_mask:0xf bank_mask:0xf
	v_mul_f32_dpp v4, v4, v4 row_shr:4 row_mask:0xf bank_mask:0xf
	v_mul_f32_dpp v5, v5, v5 row_shr:4 row_mask:0xf bank_mask:0xf
	v_mul_f32_dpp v6, v6, v6 row_shr:4 row_mask:0xf bank_mask:0xf
	v_mul_f32_dpp v7, v7, v7 row_shr:4 row_mask:0xf bank_mask:0xf

;     __device__ __forceinline__ void operator()(AccRef acc, const pg8::Unit& u, int wr, int wc, int fr, int fq) const {
;     ...
;                     GATE_SCAN_STEP(1); GATE_SCAN_STEP(2); GATE_SCAN_STEP(4); GATE_SCAN_STEP(8);
	v_lshl_add_u64 v[26:27], s[6:7], 0, v[24:25]
	s_nop 1
	v_fmac_f32_dpp v12, v12, v8 row_shr:8 row_mask:0xf bank_mask:0xf
	v_fmac_f32_dpp v13, v13, v9 row_shr:8 row_mask:0xf bank_mask:0xf
	v_fmac_f32_dpp v14, v14, v10 row_shr:8 row_mask:0xf bank_mask:0xf
	v_fmac_f32_dpp v15, v15, v11 row_shr:8 row_mask:0xf bank_mask:0xf
	v_fmac_f32_dpp v16, v16, v4 row_shr:8 row_mask:0xf bank_mask:0xf
	v_fmac_f32_dpp v17, v17, v5 row_shr:8 row_mask:0xf bank_mask:0xf
	v_fmac_f32_dpp v18, v18, v6 row_shr:8 row_mask:0xf bank_mask:0xf
	v_fmac_f32_dpp v19, v19, v7 row_shr:8 row_mask:0xf bank_mask:0xf
	v_mul_f32_dpp v8, v8, v8 row_shr:8 row_mask:0xf bank_mask:0xf
	v_mul_f32_dpp v9, v9, v9 row_shr:8 row_mask:0xf bank_mask:0xf
	v_mul_f32_dpp v10, v10, v10 row_shr:8 row_mask:0xf bank_mask:0xf
	v_mul_f32_dpp v11, v11, v11 row_shr:8 row_mask:0xf bank_mask:0xf
	v_mul_f32_dpp v4, v4, v4 row_shr:8 row_mask:0xf bank_mask:0xf
	v_mul_f32_dpp v5, v5, v5 row_shr:8 row_mask:0xf bank_mask:0xf
	v_mul_f32_dpp v6, v6, v6 row_shr:8 row_mask:0xf bank_mask:0xf
	v_mul_f32_dpp v7, v7, v7 row_shr:8 row_mask:0xf bank_mask:0xf

;     __device__ __forceinline__ void operator()(AccRef acc, const pg8::Unit& u, int wr, int wc, int fr, int fq) const {
;     ...
; #pragma unroll
;                     for (int q = 0; q < 4; ++q) {
;                         const float A1 = __int_as_float(__builtin_amdgcn_ds_bpermute(l15, __float_as_int(A[q]))), H1 = __int_as_float(__builtin_amdgcn_ds_bpermute(l15, __float_as_int(B[q])));
;                         B[4 + q] = fmaf(A[4 + q], H1, B[4 + q]); A[4 + q] *= A1; }
; #pragma unroll
;                     for (int sg = 0; sg < 2; ++sg) { const size_t ro = (size_t)(row0 + ai * 128 + (2 * mp + sg) * 16) * RW + ch;
;                         *(f32x4*)(SA + ro) = (f32x4){A[sg * 4], A[sg * 4 + 1], A[sg * 4 + 2], A[sg * 4 + 3]}; *(f32x4*)(SB + ro) = (f32x4){B[sg * 4], B[sg * 4 + 1], B[sg * 4 + 2], B[sg * 4 + 3]}; }
;                     if (fr == 15) { const size_t so = (size_t)(u.pm * 8 + ai * 4 + wr * 2 + mp) * RW + ch;
;                         *(f32x4*)(sumA + so) = (f32x4){A[4], A[5], A[6], A[7]}; *(f32x4*)(sumH + so) = (f32x4){B[4], B[5], B[6], B[7]}; }
	ds_bpermute_b32 v0, v168, v8
	ds_bpermute_b32 v20, v168, v12
	ds_bpermute_b32 v1, v168, v9
	ds_bpermute_b32 v21, v168, v13
	ds_bpermute_b32 v2, v168, v10
	ds_bpermute_b32 v22, v168, v14
	ds_bpermute_b32 v3, v168, v11
	ds_bpermute_b32 v23, v168, v15
	global_store_dwordx4 v[26:27], v[8:11], off
	s_waitcnt lgkmcnt(0)
	v_pk_mul_f32 v[0:1], v[4:5], v[0:1]
	v_pk_fma_f32 v[4:5], v[4:5], v[20:21], v[16:17]
	v_lshl_add_u64 v[8:9], s[8:9], 0, v[24:25]
	global_store_dwordx4 v[8:9], v[12:15], off
	v_lshl_add_u64 v[8:9], v[82:83], 0, v[84:85]
	v_lshlrev_b64 v[8:9], 2, v[8:9]
	v_pk_mul_f32 v[2:3], v[6:7], v[2:3]
	v_lshl_add_u64 v[10:11], s[6:7], 0, v[8:9]
	v_pk_fma_f32 v[6:7], v[6:7], v[22:23], v[18:19]
	v_lshl_add_u64 v[8:9], s[8:9], 0, v[8:9]
	global_store_dwordx4 v[10:11], v[0:3], off
	global_store_dwordx4 v[8:9], v[4:7], off
	s_and_saveexec_b64 s[28:29], s[0:1]
	s_cbranch_execz .LBB0_597
	s_lshl_b32 s46, s46, 3
	s_add_i32 s74, s46, s97
	s_ashr_i32 s75, s74, 31
	s_lshl_b64 s[74:75], s[74:75], 9
	v_lshl_add_u64 v[8:9], s[74:75], 0, v[84:85]
	v_lshlrev_b64 v[8:9], 2, v[8:9]
	v_lshl_add_u64 v[10:11], s[18:19], 0, v[8:9]
	global_store_dwordx4 v[10:11], v[0:3], off
	s_nop 1
	v_lshl_add_u64 v[0:1], s[20:21], 0, v[8:9]
	global_store_dwordx4 v[0:1], v[4:7], off
